# MoE gate/up stream too: next unit's first tiles and token rows fetched by the previous unit's last steps
# baseline (speedup 1.0000x reference)
; #define GAS __attribute__((address_space(1)))
; #define LAS __attribute__((address_space(3)))
;     ...
;     const size_t o_hid = out_off ? out_off : WS_HID, o_yr = out_off ? out_off : WS_YR;
;     constexpr int KD = (MODE == 0) ? D : DEXP, NT = KD / 64, NSLAB = (MODE == 0) ? 8 : 16, LDW = (MODE == 0) ? DEXP : D, LDX = KD;
;     const int half = wave & 1, nb16 = lane & 15, kb = 4 * (wave >> 1) + (lane >> 4);
;     const int tk = lane & 15, q = lane >> 4;
;     const GAS char* wmat = (const GAS char*)((MODE == 0) ? (half ? a.inp(I_WEU) : a.inp(I_WEG)) : a.inp(I_WED));
;     const unsigned wvo = (unsigned)((4 * kb * LDW + 4 * nb16) * 4);
;     const int lw0 = (64 * half + 4 * nb16) * 128 + (((kb >> 1) ^ ((2 * nb16) & 7)) << 4) + (kb & 1) * 8, lw1 = lw0 ^ 16;
;     const int rd_g = (tk >> 1) & 7;
;     for (int vb = bid; vb < NEXP * NSLAB; vb += G) {
;         const int xcd = vb & 7, idx = vb >> 3; const int e = xcd * 8 + idx / NSLAB, slab = idx % NSLAB;
;         const int M = __builtin_amdgcn_readfirstlane(lc[LC_CNT / 4 + e]), row0 = __builtin_amdgcn_readfirstlane(lc[LC_PSTART / 4 + e]);
;         const size_t wuo = (MODE == 0) ? ((size_t)(l * NEXP + e) * D * DEXP + slab * 64) * 4 : ((size_t)(l * NEXP + e) * DEXP * D + slab * 128 + 64 * half) * 4;
;         const __amdgpu_buffer_rsrc_t wrs = __builtin_amdgcn_make_buffer_rsrc((void*)(wmat + wuo), 0, KD * LDW * 4, 0x00020000);
;         const __amdgpu_buffer_rsrc_t xrs = __builtin_amdgcn_make_buffer_rsrc((MODE == 0) ? (void*)(ws + WS_U) : (void*)((const GAS char*)(ws + WS_HID) + (size_t)row0 * LDX * 2), 0, 0x7fffffff, 0x00020000);
;         const int* el = (const int*)(ws + WS_ELIST) + (size_t)e * T;
;         for (int rp = 0; rp < M; rp += 384) {
;             unsigned xso[6];
; #pragma unroll
;             for (int i = 0; i < 6; ++i) { int tok = rp + wave * 48 + 8 * i + (lane >> 3); tok = min(tok, M - 1); if (VAR == 5) tok &= 15; if (MODE == 0) tok = el[tok]; xso[i] = (unsigned)(tok * LDX * 2 + (lane & 7) * 16); }
;             LAS unsigned char* xw = lds + MS_XOFF + wave * MS_XWAVE; const int xwo = (lane >> 3) * 128 + (((lane & 7) ^ ((lane >> 4) & 3)) << 4);
;             const LAS unsigned char* xr = lds + MS_XOFF + wave * MS_XWAVE + tk * 128 + ((q ^ rd_g) << 4);
.LBB0_1713:
	s_or_b64 exec, exec, s[12:13]
	s_cmpk_gt_i32 s3, 0x1ff
	s_waitcnt lgkmcnt(0)
	s_barrier
	s_cbranch_scc1 .LBB0_1727
	s_mov_b32 s83, 0
	s_mov_b32 s10, 0x7ffffff0
	s_ashr_i32 s12, s0, 6
	s_and_b32 s7, s12, 1
	s_lshl_b32 s0, s12, 1
	v_bfe_u32 v4, v2, 4, 2
	v_and_or_b32 v5, s0, -4, v4
	s_cmp_eq_u32 s7, 0
	s_movk_i32 s0, 0xe8
	s_cselect_b32 s0, s0, 0xf0
	v_and_b32_e32 v3, 15, v2
	s_add_u32 s0, s4, s0
	s_addc_u32 s1, s5, 0
	s_waitcnt vmcnt(0)
	v_lshlrev_b32_e32 v6, 4, v3
	v_lshlrev_b32_e32 v90, 3, v4
	s_load_dwordx2 s[38:39], s[0:1], 0x0
	v_lshl_or_b32 v160, v5, 13, v6
	v_lshlrev_b32_e32 v6, 9, v3
	s_lshl_b32 s0, s7, 13
	v_and_b32_e32 v7, 8, v90
	v_or3_b32 v6, v7, v6, s0
	v_readlane_b32 s0, v255, 30
	s_lshl_b32 s24, s0, 6
	s_add_u32 s4, s8, 0x4300000
	v_lshrrev_b32_e32 v5, 1, v5
	v_lshlrev_b32_e32 v8, 1, v2
	s_addc_u32 s0, s9, 0
	v_bitop3_b32 v5, v5, v8, 6 bitop3:0x78
	s_and_b32 s5, s0, 0xffff
	s_mul_i32 s0, s12, 16
	s_mul_i32 s80, s12, 16
	v_bfe_u32 v8, v2, 3, 3
	v_or_b32_e32 v162, s0, v8
	v_lshlrev_b32_e32 v8, 4, v2
	v_and_b32_e32 v163, 0x70, v8
	v_bitop3_b32 v8, v4, v2, 7 bitop3:0x78
	v_lshl_add_u32 v161, v5, 4, v6
	v_lshrrev_b32_e32 v6, 1, v2
	v_bfe_u32 v7, v2, 1, 3
	s_add_u32 s25, s8, 0x39e61600
	s_mulk_i32 s12, 0x3000
	v_and_or_b32 v2, v2, 56, v8
	v_readlane_b32 s1, v255, 31
	s_addc_u32 s26, s9, 0
	s_add_i32 s27, s12, 0
	v_lshlrev_b32_e32 v172, 4, v2
	v_lshlrev_b32_e32 v2, 7, v3
	v_add_u32_e32 v173, s27, v2
	v_add_u32_e32 v176, 0, v2
	v_or_b32_e32 v177, s0, v3
	v_lshl_add_u64 v[2:3], s[8:9], 0, v[90:91]
	s_mov_b64 s[0:1], 0x2fe31000
	v_xor_b32_e32 v5, 16, v161
	v_bitop3_b32 v6, v6, v4, 7 bitop3:0x6c
	v_bitop3_b32 v4, v4, v7, 4 bitop3:0x36
	v_lshl_add_u64 v[156:157], v[2:3], 0, s[0:1]
	v_xor_b32_e32 v2, 64, v172
	s_mov_b32 s7, s11
	v_lshlrev_b32_e32 v174, 4, v6
	v_lshlrev_b32_e32 v175, 4, v4
	v_or_b32_e32 v90, 0x800, v160
	v_or_b32_e32 v178, 0x1000, v160
	v_or_b32_e32 v179, 0x1800, v160
	v_add_u32_e32 v180, 0, v5
	v_add_u32_e32 v181, s27, v2
	s_branch .LBB0_1716

; #define GAS __attribute__((address_space(1)))
; #define LAS __attribute__((address_space(3)))
; #define MS_WLOAD(set, t) do { _Pragma("unroll") for (int r_ = 0; r_ < 4; ++r_) wr[set][r_] = __builtin_bit_cast(f32x4, __builtin_amdgcn_raw_buffer_load_b128(wrs, (int)wvo + r_ * LDW * 4, MS_CL(t) * (64 * LDW * 4), 0)); } while (0)
;     ...
;     for (int vb = bid; vb < NEXP * NSLAB; vb += G) {
;         const int xcd = vb & 7, idx = vb >> 3; const int e = xcd * 8 + idx / NSLAB, slab = idx % NSLAB;
;         const int M = __builtin_amdgcn_readfirstlane(lc[LC_CNT / 4 + e]), row0 = __builtin_amdgcn_readfirstlane(lc[LC_PSTART / 4 + e]);
;         const size_t wuo = (MODE == 0) ? ((size_t)(l * NEXP + e) * D * DEXP + slab * 64) * 4 : ((size_t)(l * NEXP + e) * DEXP * D + slab * 128 + 64 * half) * 4;
;         const __amdgpu_buffer_rsrc_t wrs = __builtin_amdgcn_make_buffer_rsrc((void*)(wmat + wuo), 0, KD * LDW * 4, 0x00020000);
;         const __amdgpu_buffer_rsrc_t xrs = __builtin_amdgcn_make_buffer_rsrc((MODE == 0) ? (void*)(ws + WS_U) : (void*)((const GAS char*)(ws + WS_HID) + (size_t)row0 * LDX * 2), 0, 0x7fffffff, 0x00020000);
;         const int* el = (const int*)(ws + WS_ELIST) + (size_t)e * T;
;         for (int rp = 0; rp < M; rp += 384) {
;             unsigned xso[6];
; #pragma unroll
;             for (int i = 0; i < 6; ++i) { int tok = rp + wave * 48 + 8 * i + (lane >> 3); tok = min(tok, M - 1); if (VAR == 5) tok &= 15; if (MODE == 0) tok = el[tok]; xso[i] = (unsigned)(tok * LDX * 2 + (lane & 7) * 16); }
;             LAS unsigned char* xw = lds + MS_XOFF + wave * MS_XWAVE; const int xwo = (lane >> 3) * 128 + (((lane & 7) ^ ((lane >> 4) & 3)) << 4);
;             const LAS unsigned char* xr = lds + MS_XOFF + wave * MS_XWAVE + tk * 128 + ((q ^ rd_g) << 4);
;             f32x4 acc[3][8];
; #pragma unroll
;             for (int mt = 0; mt < 3; ++mt)
; #pragma unroll
;                 for (int j = 0; j < 8; ++j) acc[mt][j] = (f32x4){0.f, 0.f, 0.f, 0.f};
;             f32x4 wr[2][4];
;             bf16x8 xs[6];
;     ...
;             const LAS unsigned char* xr1 = lds + MS_XOFF + wave * MS_XWAVE + tk * 128 + (((4 + q) ^ rd_g) << 4);
;             __syncthreads();
;             MS_XSLOAD(0); MS_WLOAD(0, 0); MS_WLOAD(1, 1);
;             MS_WCOMMIT(0, 0); MS_WLOAD(0, 2);
;             MS_XSWRITE(0); MS_XSLOAD(1);
;             __syncthreads();
.LBB0_1716:
	s_ashr_i32 s1, s3, 3
	s_lshr_b32 s8, s1, 29
	s_lshl_b32 s0, s3, 3
	s_add_i32 s8, s1, s8
	s_and_b32 s0, s0, 56
	s_ashr_i32 s8, s8, 3
	s_add_i32 s0, s0, s8
	s_lshl_b32 s9, s0, 2
	s_add_i32 s9, s9, 0
	s_add_i32 s9, s9, 0x20000
	v_mov_b32_e32 v2, s9
	v_mov_b32_e32 v4, s9
	ds_read2_b32 v[2:3], v2 offset0:136 offset1:200
	ds_read2_b32 v[4:5], v4 offset0:140 offset1:204
	s_add_i32 s91, s3, 0x100
	s_waitcnt lgkmcnt(0)
	v_readfirstlane_b32 s28, v3
	v_readfirstlane_b32 s29, v2
	v_readfirstlane_b32 s89, v5
	s_cmpk_gt_i32 s91, 0x1ff
	s_cselect_b32 s89, 0, s89
	s_cmpk_lg_i32 s2, 0x100
	s_cselect_b32 s89, 0, s89
	s_cmp_lt_i32 s28, 1
	s_cbranch_scc1 .LBB0_1715
	s_lshl_b32 s8, s8, 3
	s_sub_i32 s1, s1, s8
	s_add_i32 s8, s0, s24
	s_lshl_b32 s12, s1, 6
	s_ashr_i32 s9, s8, 31
	s_ashr_i32 s13, s12, 31
	s_lshl_b64 s[8:9], s[8:9], 22
	s_lshl_b64 s[30:31], s[12:13], 2
	s_add_u32 s1, s38, s8
	s_addc_u32 s9, s39, s9
	s_add_u32 s8, s1, s30
	s_addc_u32 s1, s9, s31
	s_and_b32 s9, s1, 0xffff
	s_mul_hi_i32 s1, s0, 0x8100
	s_mul_i32 s0, s0, 0x8100
	s_add_u32 s40, s25, s0
	s_addc_u32 s41, s26, s1
	s_add_i32 s30, s28, -1
	v_lshl_add_u64 v[158:159], s[12:13], 1, v[156:157]
	s_mov_b32 s31, 0
	s_branch .LBB0_1719
.LBB0_1718:
	s_or_b64 exec, exec, s[12:13]
	s_mov_b32 s83, s84
	s_addk_i32 s31, 0x180
	s_cmp_ge_i32 s31, s28
	s_cbranch_scc1 .LBB0_1715
.LBB0_1719:
	s_add_i32 s87, s31, 0x180
	s_cmp_lt_i32 s87, s28
	s_cbranch_scc1 .Lxk_same
	s_cmp_lt_i32 s89, 1
	s_cbranch_scc1 .Lxk_none
	s_mov_b32 s84, 1
	s_add_i32 s86, s89, -1
	s_mov_b32 s87, 0
	s_add_u32 s42, s40, 0x20400
	s_addc_u32 s43, s41, 0
	s_mov_b32 s85, 0x1000000
	s_branch .Lxk_sel
.Lxk_same:
	s_mov_b32 s84, 1
	s_mov_b32 s86, s30
	s_mov_b64 s[42:43], s[40:41]
	s_mov_b32 s85, 0
	s_branch .Lxk_sel
.Lxk_none:
	s_mov_b32 s84, 0
	s_mov_b32 s85, 0x3a0000
	s_mov_b32 s86, 0
	s_mov_b32 s87, 0
	s_mov_b64 s[42:43], s[40:41]
	s_branch .Lxk_nel
.Lxk_sel:
	v_add_u32_e32 v5, s87, v162
	v_min_i32_e32 v6, s86, v5
	v_ashrrev_i32_e32 v7, 31, v6
	v_lshl_add_u64 v[6:7], v[6:7], 2, s[42:43]
	global_load_dword v246, v[6:7], off
	v_or_b32_e32 v6, 8, v5
	v_min_i32_e32 v6, s86, v6
	v_ashrrev_i32_e32 v7, 31, v6
	v_lshl_add_u64 v[6:7], v[6:7], 2, s[42:43]
	global_load_dword v247, v[6:7], off
	v_add_u32_e32 v6, 0x80, v5
	v_min_i32_e32 v6, s86, v6
	v_ashrrev_i32_e32 v7, 31, v6
	v_lshl_add_u64 v[6:7], v[6:7], 2, s[42:43]
	global_load_dword v248, v[6:7], off
	v_add_u32_e32 v6, 0x88, v5
	v_min_i32_e32 v6, s86, v6
	v_ashrrev_i32_e32 v7, 31, v6
	v_lshl_add_u64 v[6:7], v[6:7], 2, s[42:43]
	global_load_dword v249, v[6:7], off
	v_add_u32_e32 v6, 0x100, v5
	v_min_i32_e32 v6, s86, v6
	v_ashrrev_i32_e32 v7, 31, v6
	v_lshl_add_u64 v[6:7], v[6:7], 2, s[42:43]
	global_load_dword v250, v[6:7], off
	v_add_u32_e32 v6, 0x108, v5
	v_min_i32_e32 v6, s86, v6
	v_ashrrev_i32_e32 v7, 31, v6
	v_lshl_add_u64 v[6:7], v[6:7], 2, s[42:43]
	global_load_dword v251, v[6:7], off
.Lxk_nel:
	s_cmp_eq_u32 s83, 1
	s_cbranch_scc1 .Lxk_fast
	v_add_u32_e32 v4, s31, v162
	v_min_i32_e32 v2, s30, v4
	v_ashrrev_i32_e32 v3, 31, v2
	v_lshl_add_u64 v[2:3], v[2:3], 2, s[40:41]
	global_load_dword v182, v[2:3], off
	v_or_b32_e32 v2, 8, v4
	v_min_i32_e32 v2, s30, v2
	v_ashrrev_i32_e32 v3, 31, v2
	v_lshl_add_u64 v[2:3], v[2:3], 2, s[40:41]
	global_load_dword v183, v[2:3], off
	v_add_u32_e32 v2, 0x80, v4
	v_min_i32_e32 v2, s30, v2
	v_ashrrev_i32_e32 v3, 31, v2
	v_lshl_add_u64 v[2:3], v[2:3], 2, s[40:41]
	global_load_dword v184, v[2:3], off
	v_add_u32_e32 v2, 0x88, v4
	v_min_i32_e32 v2, s30, v2
	v_ashrrev_i32_e32 v3, 31, v2
	v_lshl_add_u64 v[2:3], v[2:3], 2, s[40:41]
	global_load_dword v185, v[2:3], off
	v_add_u32_e32 v2, 0x100, v4
	v_min_i32_e32 v2, s30, v2
	v_ashrrev_i32_e32 v3, 31, v2
	v_lshl_add_u64 v[2:3], v[2:3], 2, s[40:41]
	global_load_dword v186, v[2:3], off
	v_add_u32_e32 v2, 0x108, v4
	v_min_i32_e32 v2, s30, v2
	v_ashrrev_i32_e32 v3, 31, v2
	v_lshl_add_u64 v[2:3], v[2:3], 2, s[40:41]
	global_load_dword v187, v[2:3], off
	v_add_u32_e32 v188, 0, v161
	v_add_u32_e32 v189, s27, v172
	s_mov_b32 s0, -2
	s_barrier
	s_waitcnt vmcnt(0)
	v_lshl_or_b32 v182, v182, 12, v163
	v_lshl_or_b32 v183, v183, 12, v163
	v_lshl_or_b32 v184, v184, 12, v163
	v_lshl_or_b32 v185, v185, 12, v163
	v_lshl_or_b32 v186, v186, 12, v163
	v_lshl_or_b32 v187, v187, 12, v163
	buffer_load_dwordx4 v[2:5], v182, s[4:7], 0 offen
	buffer_load_dwordx4 v[6:9], v183, s[4:7], 0 offen
	buffer_load_dwordx4 v[10:13], v184, s[4:7], 0 offen
	buffer_load_dwordx4 v[14:17], v185, s[4:7], 0 offen
	buffer_load_dwordx4 v[18:21], v186, s[4:7], 0 offen
	buffer_load_dwordx4 v[22:25], v187, s[4:7], 0 offen
	buffer_load_dwordx4 v[26:29], v160, s[8:11], 0 offen nt
	buffer_load_dwordx4 v[30:33], v90, s[8:11], 0 offen nt
	buffer_load_dwordx4 v[34:37], v178, s[8:11], 0 offen nt
	buffer_load_dwordx4 v[38:41], v179, s[8:11], 0 offen nt
	buffer_load_dwordx4 v[74:77], v160, s[8:11], s11 offen nt
	buffer_load_dwordx4 v[78:81], v90, s[8:11], s11 offen nt
	buffer_load_dwordx4 v[82:85], v178, s[8:11], s11 offen nt
	buffer_load_dwordx4 v[86:89], v179, s[8:11], s11 offen nt
	s_waitcnt vmcnt(6)
	v_cvt_pk_bf16_f32 v42, v26, v30
	v_cvt_pk_bf16_f32 v26, v27, v31
	s_waitcnt vmcnt(4)
; #define LAS __attribute__((address_space(3)))
; #define MS_WLOAD(set, t) do { _Pragma("unroll") for (int r_ = 0; r_ < 4; ++r_) wr[set][r_] = __builtin_bit_cast(f32x4, __builtin_amdgcn_raw_buffer_load_b128(wrs, (int)wvo + r_ * LDW * 4, MS_CL(t) * (64 * LDW * 4), 0)); } while (0)
; #define MS_WCOMMIT(set, bufi) do { LAS unsigned char* wb_ = lds + (bufi) * MS_TILE; _Pragma("unroll") for (int i_ = 0; i_ < 4; ++i_) { \
;             u32x2 p_; p_.x = pk2(wr[set][0][i_], wr[set][1][i_]); p_.y = pk2(wr[set][2][i_], wr[set][3][i_]); \
;             *(LAS u32x2*)(wb_ + ((i_ < 2) ? lw0 : lw1) + i_ * 128) = p_; } } while (0)
; #define MS_XSLOAD(t) do { _Pragma("unroll") for (int i_ = 0; i_ < 6; ++i_) xs[i_] = __builtin_bit_cast(bf16x8, __builtin_amdgcn_raw_buffer_load_b128(xrs, (int)xso[i_], MS_CL(t) * 128, 0)); } while (0)
; #define MS_XSWRITE(bufi) do { _Pragma("unroll") for (int i_ = 0; i_ < 6; ++i_) *(LAS bf16x8*)(xw + (bufi) * MS_XBUF + i_ * 1024 + ((i_ & 1) ? (xwo ^ 64) : xwo)) = xs[i_]; } while (0)
; #define MS_STEP(I, J, t) do { MS_WCOMMIT(J, J); MS_WLOAD(J, (t) + 3); MS_COMPUTE(I); MS_XSWRITE(J); MS_XSLOAD((t) + 2); __syncthreads(); } while (0)
;     ...
;             f32x4 acc[3][8];
; #pragma unroll
;             for (int mt = 0; mt < 3; ++mt)
; #pragma unroll
;                 for (int j = 0; j < 8; ++j) acc[mt][j] = (f32x4){0.f, 0.f, 0.f, 0.f};
;             f32x4 wr[2][4];
;             bf16x8 xs[6];
;     ...
;             const LAS unsigned char* xr1 = lds + MS_XOFF + wave * MS_XWAVE + tk * 128 + (((4 + q) ^ rd_g) << 4);
;             __syncthreads();
;             MS_XSLOAD(0); MS_WLOAD(0, 0); MS_WLOAD(1, 1);
;             MS_WCOMMIT(0, 0); MS_WLOAD(0, 2);
;             MS_XSWRITE(0); MS_XSLOAD(1);
;             __syncthreads();
; #pragma unroll 1
;             for (int t = 0; t < NT; t += 2) { MS_STEP(0, 1, t); MS_STEP(1, 0, t + 1); }
	v_cvt_pk_bf16_f32 v43, v34, v38
	v_cvt_pk_bf16_f32 v27, v35, v39
	ds_write2_b64 v188, v[42:43], v[26:27] offset1:16
	v_cvt_pk_bf16_f32 v26, v28, v32
	v_cvt_pk_bf16_f32 v27, v36, v40
	v_cvt_pk_bf16_f32 v28, v29, v33
	v_cvt_pk_bf16_f32 v29, v37, v41
	ds_write2_b64 v180, v[26:27], v[28:29] offset0:32 offset1:48
	buffer_load_dwordx4 v[96:99], v160, s[8:11], s22 offen nt
	buffer_load_dwordx4 v[100:103], v90, s[8:11], s22 offen nt
	buffer_load_dwordx4 v[104:107], v178, s[8:11], s22 offen nt
	buffer_load_dwordx4 v[108:111], v179, s[8:11], s22 offen nt
	ds_write_b128 v189, v[2:5] offset:32768
	ds_write_b128 v181, v[6:9] offset:33792
	ds_write_b128 v189, v[10:13] offset:34816
	ds_write_b128 v181, v[14:17] offset:35840
	ds_write_b128 v189, v[18:21] offset:36864
	ds_write_b128 v181, v[22:25] offset:37888
	buffer_load_dwordx4 v[132:135], v182, s[4:7], s92 offen
	buffer_load_dwordx4 v[124:127], v183, s[4:7], s92 offen
	buffer_load_dwordx4 v[140:143], v184, s[4:7], s92 offen
	buffer_load_dwordx4 v[144:147], v185, s[4:7], s92 offen
	buffer_load_dwordx4 v[128:131], v186, s[4:7], s92 offen
	buffer_load_dwordx4 v[136:139], v187, s[4:7], s92 offen
	v_mov_b32_e32 v2, 0
	v_mov_b32_e32 v3, v2
	v_mov_b32_e32 v4, v2
	v_mov_b32_e32 v5, v2
	v_mov_b32_e32 v10, v2
	v_mov_b32_e32 v11, v2
	v_mov_b32_e32 v12, v2
	v_mov_b32_e32 v13, v2
	v_mov_b32_e32 v18, v2
	v_mov_b32_e32 v19, v2
	v_mov_b32_e32 v20, v2
	v_mov_b32_e32 v21, v2
	v_mov_b32_e32 v26, v2
	v_mov_b32_e32 v27, v2
	v_mov_b32_e32 v28, v2
	v_mov_b32_e32 v29, v2
	v_mov_b32_e32 v6, v2
	v_mov_b32_e32 v7, v2
	v_mov_b32_e32 v8, v2
	v_mov_b32_e32 v9, v2
	v_mov_b32_e32 v14, v2
	v_mov_b32_e32 v15, v2
	v_mov_b32_e32 v16, v2
	v_mov_b32_e32 v17, v2
	v_mov_b32_e32 v22, v2
	v_mov_b32_e32 v23, v2
	v_mov_b32_e32 v24, v2
	v_mov_b32_e32 v25, v2
	v_mov_b32_e32 v30, v2
	v_mov_b32_e32 v31, v2
	v_mov_b32_e32 v32, v2
	v_mov_b32_e32 v33, v2
	v_mov_b32_e32 v34, v2
	v_mov_b32_e32 v35, v2
	v_mov_b32_e32 v36, v2
	v_mov_b32_e32 v37, v2
	v_mov_b32_e32 v42, v2
	v_mov_b32_e32 v43, v2
	v_mov_b32_e32 v44, v2
	v_mov_b32_e32 v45, v2
	v_mov_b32_e32 v50, v2
	v_mov_b32_e32 v51, v2
	v_mov_b32_e32 v52, v2
	v_mov_b32_e32 v53, v2
	v_mov_b32_e32 v58, v2
	v_mov_b32_e32 v59, v2
	v_mov_b32_e32 v60, v2
	v_mov_b32_e32 v61, v2
	v_mov_b32_e32 v38, v2
	v_mov_b32_e32 v39, v2
	v_mov_b32_e32 v40, v2
	v_mov_b32_e32 v41, v2
	v_mov_b32_e32 v46, v2
	v_mov_b32_e32 v47, v2
	v_mov_b32_e32 v48, v2
	v_mov_b32_e32 v49, v2
	v_mov_b32_e32 v54, v2
	v_mov_b32_e32 v55, v2
	v_mov_b32_e32 v56, v2
	v_mov_b32_e32 v57, v2
	v_mov_b32_e32 v62, v2
	v_mov_b32_e32 v63, v2
	v_mov_b32_e32 v64, v2
	v_mov_b32_e32 v65, v2
	v_mov_b32_e32 v66, v2
	v_mov_b32_e32 v67, v2
	v_mov_b32_e32 v68, v2
	v_mov_b32_e32 v69, v2
	v_mov_b32_e32 v92, v2
	v_mov_b32_e32 v93, v2
	v_mov_b32_e32 v94, v2
	v_mov_b32_e32 v95, v2
	v_mov_b32_e32 v116, v2
	v_mov_b32_e32 v117, v2
	v_mov_b32_e32 v118, v2
	v_mov_b32_e32 v119, v2
	v_mov_b32_e32 v148, v2
	v_mov_b32_e32 v149, v2
	v_mov_b32_e32 v150, v2
	v_mov_b32_e32 v151, v2
	v_mov_b32_e32 v70, v2
	v_mov_b32_e32 v71, v2
	v_mov_b32_e32 v72, v2
	v_mov_b32_e32 v73, v2
	v_mov_b32_e32 v112, v2
	v_mov_b32_e32 v113, v2
	v_mov_b32_e32 v114, v2
	v_mov_b32_e32 v115, v2
	v_mov_b32_e32 v120, v2
	v_mov_b32_e32 v121, v2
	v_mov_b32_e32 v122, v2
	v_mov_b32_e32 v123, v2
	v_mov_b32_e32 v152, v2
	v_mov_b32_e32 v153, v2
	v_mov_b32_e32 v154, v2
	v_mov_b32_e32 v155, v2
	s_waitcnt lgkmcnt(0)
	s_barrier
.Lxk_disp:
	s_sub_i32 s81, s28, s31
	s_add_i32 s82, s80, 0x100
	s_cmp_gt_i32 s81, s82
	s_cbranch_scc1 .LBB0_1720
	s_cmp_eq_u32 s84, 0
	s_cbranch_scc1 .Lmoe_k_b
	s_add_i32 s81, s86, 1
	s_sub_i32 s81, s81, s87
	s_cmp_le_i32 s81, s82
	s_cbranch_scc1 .Lmoe_k_b
.LBB0_1720:
	s_add_i32 s0, s0, 2
	s_min_u32 s1, s0, 28
	s_lshl_b32 s12, s1, 17
	s_add_i32 s12, s12, 0x60000
	s_add_i32 s58, s85, 0x20000
	s_cmp_gt_u32 s0, 28
	s_cselect_b32 s12, s58, s12
	s_waitcnt vmcnt(12)
	v_cvt_pk_bf16_f32 v164, v74, v78
	s_waitcnt vmcnt(10)
	v_cvt_pk_bf16_f32 v165, v82, v86
	v_cvt_pk_bf16_f32 v166, v75, v79
	v_cvt_pk_bf16_f32 v167, v83, v87
	v_cvt_pk_bf16_f32 v190, v76, v80
	v_cvt_pk_bf16_f32 v191, v84, v88
	v_cvt_pk_bf16_f32 v192, v77, v81
	v_cvt_pk_bf16_f32 v193, v85, v89
	buffer_load_dwordx4 v[74:77], v160, s[8:11], s12 offen nt
	buffer_load_dwordx4 v[78:81], v90, s[8:11], s12 offen nt
	buffer_load_dwordx4 v[82:85], v178, s[8:11], s12 offen nt
	buffer_load_dwordx4 v[86:89], v179, s[8:11], s12 offen nt
	v_add_u32_e32 v194, 0x4000, v188
	v_add_u32_e32 v195, 0x4000, v180
	v_add_u32_e32 v214, v173, v174
	ds_write2_b64 v194, v[164:165], v[166:167] offset1:16
	ds_write2_b64 v195, v[190:191], v[192:193] offset0:32 offset1:48
	v_add_u32_e32 v215, v176, v174
	ds_read_b128 v[164:167], v214 offset:32768
	ds_read_b128 v[190:193], v214 offset:34816
	ds_read_b128 v[194:197], v214 offset:36864
	ds_read_b128 v[198:201], v215
	ds_read_b128 v[202:205], v215 offset:2048
	ds_read_b128 v[206:209], v215 offset:4096
	ds_read_b128 v[210:213], v215 offset:6144
	s_waitcnt lgkmcnt(3)
	v_mfma_f32_16x16x32_bf16 v[152:155], v[198:201], v[164:167], v[152:155]
	v_mfma_f32_16x16x32_bf16 v[62:65], v[198:201], v[190:193], v[62:65]
	v_mfma_f32_16x16x32_bf16 v[30:33], v[198:201], v[194:197], v[30:33]
	s_waitcnt lgkmcnt(2)
	v_mfma_f32_16x16x32_bf16 v[120:123], v[202:205], v[164:167], v[120:123]
	v_mfma_f32_16x16x32_bf16 v[54:57], v[202:205], v[190:193], v[54:57]
	v_mfma_f32_16x16x32_bf16 v[22:25], v[202:205], v[194:197], v[22:25]
	s_waitcnt lgkmcnt(1)
	v_mfma_f32_16x16x32_bf16 v[112:115], v[206:209], v[164:167], v[112:115]
	v_mfma_f32_16x16x32_bf16 v[46:49], v[206:209], v[190:193], v[46:49]
	v_mfma_f32_16x16x32_bf16 v[14:17], v[206:209], v[194:197], v[14:17]
	s_waitcnt lgkmcnt(0)
; #define LAS __attribute__((address_space(3)))
; #define MS_WLOAD(set, t) do { _Pragma("unroll") for (int r_ = 0; r_ < 4; ++r_) wr[set][r_] = __builtin_bit_cast(f32x4, __builtin_amdgcn_raw_buffer_load_b128(wrs, (int)wvo + r_ * LDW * 4, MS_CL(t) * (64 * LDW * 4), 0)); } while (0)
; #define MS_WCOMMIT(set, bufi) do { LAS unsigned char* wb_ = lds + (bufi) * MS_TILE; _Pragma("unroll") for (int i_ = 0; i_ < 4; ++i_) { \
;             u32x2 p_; p_.x = pk2(wr[set][0][i_], wr[set][1][i_]); p_.y = pk2(wr[set][2][i_], wr[set][3][i_]); \
;             *(LAS u32x2*)(wb_ + ((i_ < 2) ? lw0 : lw1) + i_ * 128) = p_; } } while (0)
; #define MS_XSLOAD(t) do { _Pragma("unroll") for (int i_ = 0; i_ < 6; ++i_) xs[i_] = __builtin_bit_cast(bf16x8, __builtin_amdgcn_raw_buffer_load_b128(xrs, (int)xso[i_], MS_CL(t) * 128, 0)); } while (0)
; #define MS_XSWRITE(bufi) do { _Pragma("unroll") for (int i_ = 0; i_ < 6; ++i_) *(LAS bf16x8*)(xw + (bufi) * MS_XBUF + i_ * 1024 + ((i_ & 1) ? (xwo ^ 64) : xwo)) = xs[i_]; } while (0)
; #define MS_STEP(I, J, t) do { MS_WCOMMIT(J, J); MS_WLOAD(J, (t) + 3); MS_COMPUTE(I); MS_XSWRITE(J); MS_XSLOAD((t) + 2); __syncthreads(); } while (0)
;     ...
;             const LAS unsigned char* xr1 = lds + MS_XOFF + wave * MS_XWAVE + tk * 128 + (((4 + q) ^ rd_g) << 4);
;             __syncthreads();
;             MS_XSLOAD(0); MS_WLOAD(0, 0); MS_WLOAD(1, 1);
;             MS_WCOMMIT(0, 0); MS_WLOAD(0, 2);
;             MS_XSWRITE(0); MS_XSLOAD(1);
;             __syncthreads();
; #pragma unroll 1
;             for (int t = 0; t < NT; t += 2) { MS_STEP(0, 1, t); MS_STEP(1, 0, t + 1); }
	v_mfma_f32_16x16x32_bf16 v[70:73], v[210:213], v[164:167], v[70:73]
	v_mfma_f32_16x16x32_bf16 v[38:41], v[210:213], v[190:193], v[38:41]
	v_mfma_f32_16x16x32_bf16 v[6:9], v[210:213], v[194:197], v[6:9]
	ds_read_b128 v[198:201], v215 offset:8192
	ds_read_b128 v[202:205], v215 offset:10240
	ds_read_b128 v[206:209], v215 offset:12288
	ds_read_b128 v[210:213], v215 offset:14336
	s_waitcnt lgkmcnt(3)
	v_mfma_f32_16x16x32_bf16 v[148:151], v[198:201], v[164:167], v[148:151]
	v_mfma_f32_16x16x32_bf16 v[58:61], v[198:201], v[190:193], v[58:61]
	v_mfma_f32_16x16x32_bf16 v[26:29], v[198:201], v[194:197], v[26:29]
	s_waitcnt lgkmcnt(2)
	v_mfma_f32_16x16x32_bf16 v[116:119], v[202:205], v[164:167], v[116:119]
	v_mfma_f32_16x16x32_bf16 v[50:53], v[202:205], v[190:193], v[50:53]
	v_mfma_f32_16x16x32_bf16 v[18:21], v[202:205], v[194:197], v[18:21]
	s_waitcnt lgkmcnt(1)
	v_mfma_f32_16x16x32_bf16 v[92:95], v[206:209], v[164:167], v[92:95]
	v_mfma_f32_16x16x32_bf16 v[42:45], v[206:209], v[190:193], v[42:45]
	v_mfma_f32_16x16x32_bf16 v[10:13], v[206:209], v[194:197], v[10:13]
	s_waitcnt lgkmcnt(0)
	v_mfma_f32_16x16x32_bf16 v[66:69], v[210:213], v[164:167], v[66:69]
	v_mfma_f32_16x16x32_bf16 v[34:37], v[210:213], v[190:193], v[34:37]
	v_mfma_f32_16x16x32_bf16 v[2:5], v[210:213], v[194:197], v[2:5]
	v_add_u32_e32 v216, v173, v175
	ds_read_b128 v[164:167], v216 offset:32768
	ds_read_b128 v[190:193], v216 offset:34816
	v_add_u32_e32 v217, v176, v175
	ds_read_b128 v[194:197], v216 offset:36864
	ds_read_b128 v[198:201], v217
	ds_read_b128 v[202:205], v217 offset:2048
	ds_read_b128 v[206:209], v217 offset:4096
	ds_read_b128 v[210:213], v217 offset:6144
	s_waitcnt lgkmcnt(3)
	v_mfma_f32_16x16x32_bf16 v[152:155], v[198:201], v[164:167], v[152:155]
	v_mfma_f32_16x16x32_bf16 v[62:65], v[198:201], v[190:193], v[62:65]
	v_mfma_f32_16x16x32_bf16 v[30:33], v[198:201], v[194:197], v[30:33]
	s_waitcnt lgkmcnt(2)
	v_mfma_f32_16x16x32_bf16 v[120:123], v[202:205], v[164:167], v[120:123]
	v_mfma_f32_16x16x32_bf16 v[54:57], v[202:205], v[190:193], v[54:57]
	v_mfma_f32_16x16x32_bf16 v[22:25], v[202:205], v[194:197], v[22:25]
	s_waitcnt lgkmcnt(1)
	v_mfma_f32_16x16x32_bf16 v[112:115], v[206:209], v[164:167], v[112:115]
	v_mfma_f32_16x16x32_bf16 v[46:49], v[206:209], v[190:193], v[46:49]
	v_mfma_f32_16x16x32_bf16 v[14:17], v[206:209], v[194:197], v[14:17]
	s_waitcnt lgkmcnt(0)
	v_mfma_f32_16x16x32_bf16 v[70:73], v[210:213], v[164:167], v[70:73]
	v_mfma_f32_16x16x32_bf16 v[38:41], v[210:213], v[190:193], v[38:41]
	v_mfma_f32_16x16x32_bf16 v[6:9], v[210:213], v[194:197], v[6:9]
	ds_read_b128 v[198:201], v217 offset:8192
	ds_read_b128 v[202:205], v217 offset:10240
	ds_read_b128 v[206:209], v217 offset:12288
	ds_read_b128 v[210:213], v217 offset:14336
	s_min_u32 s12, s0, 29
	s_lshl_b32 s12, s12, 7
	s_waitcnt vmcnt(9)
	ds_write_b128 v189, v[132:135] offset:38912
	s_waitcnt vmcnt(8)
	ds_write_b128 v181, v[124:127] offset:39936
	s_waitcnt vmcnt(7)
	ds_write_b128 v189, v[140:143] offset:40960
	s_waitcnt vmcnt(6)
	ds_write_b128 v181, v[144:147] offset:41984
	s_waitcnt vmcnt(5)
	ds_write_b128 v189, v[128:131] offset:43008
	s_waitcnt vmcnt(4)
	ds_write_b128 v181, v[136:139] offset:44032
	s_addk_i32 s12, 0x100
	s_cmp_lt_u32 s0, 30
	s_cbranch_scc1 .Lxk_nx0
	s_cmp_eq_u32 s84, 0
	s_cbranch_scc1 .Lxk_nx0
	s_mov_b32 s12, 0
	v_lshl_or_b32 v182, v246, 12, v163
	v_lshl_or_b32 v183, v247, 12, v163
	v_lshl_or_b32 v184, v248, 12, v163
	v_lshl_or_b32 v185, v249, 12, v163
	v_lshl_or_b32 v186, v250, 12, v163
	v_lshl_or_b32 v187, v251, 12, v163
.Lxk_nx0:
	s_waitcnt lgkmcnt(9)
	v_mfma_f32_16x16x32_bf16 v[148:151], v[198:201], v[164:167], v[148:151]
	buffer_load_dwordx4 v[124:127], v182, s[4:7], s12 offen
	buffer_load_dwordx4 v[128:131], v183, s[4:7], s12 offen
	buffer_load_dwordx4 v[132:135], v184, s[4:7], s12 offen
	buffer_load_dwordx4 v[136:139], v185, s[4:7], s12 offen
	buffer_load_dwordx4 v[140:143], v186, s[4:7], s12 offen
	buffer_load_dwordx4 v[144:147], v187, s[4:7], s12 offen
	s_min_u32 s12, s0, 27
	s_waitcnt lgkmcnt(0)
	v_mfma_f32_16x16x32_bf16 v[116:119], v[202:205], v[164:167], v[116:119]
	s_barrier
	s_lshl_b32 s12, s12, 17
	v_mfma_f32_16x16x32_bf16 v[92:95], v[206:209], v[164:167], v[92:95]
	s_add_i32 s12, s12, 0x80000
	s_sub_i32 s58, s0, 28
	s_lshl_b32 s58, s58, 17
	s_add_i32 s58, s58, s85
	s_cmp_gt_u32 s0, 27
	s_cselect_b32 s12, s58, s12
	v_mfma_f32_16x16x32_bf16 v[66:69], v[210:213], v[164:167], v[66:69]
	v_cvt_pk_bf16_f32 v164, v96, v100
	v_cvt_pk_bf16_f32 v165, v104, v108
	v_cvt_pk_bf16_f32 v96, v97, v101
	v_cvt_pk_bf16_f32 v97, v105, v109
	ds_write2_b64 v188, v[164:165], v[96:97] offset1:16
	v_cvt_pk_bf16_f32 v96, v98, v102
	v_cvt_pk_bf16_f32 v97, v106, v110
	v_cvt_pk_bf16_f32 v98, v99, v103
	v_cvt_pk_bf16_f32 v99, v107, v111
	ds_write2_b64 v180, v[96:97], v[98:99] offset0:32 offset1:48
	buffer_load_dwordx4 v[96:99], v160, s[8:11], s12 offen nt
	buffer_load_dwordx4 v[100:103], v90, s[8:11], s12 offen nt
	buffer_load_dwordx4 v[104:107], v178, s[8:11], s12 offen nt
	buffer_load_dwordx4 v[108:111], v179, s[8:11], s12 offen nt
	v_mfma_f32_16x16x32_bf16 v[58:61], v[198:201], v[190:193], v[58:61]
	v_mfma_f32_16x16x32_bf16 v[26:29], v[198:201], v[194:197], v[26:29]
	v_mfma_f32_16x16x32_bf16 v[50:53], v[202:205], v[190:193], v[50:53]
	v_mfma_f32_16x16x32_bf16 v[18:21], v[202:205], v[194:197], v[18:21]
	v_mfma_f32_16x16x32_bf16 v[42:45], v[206:209], v[190:193], v[42:45]
	v_mfma_f32_16x16x32_bf16 v[10:13], v[206:209], v[194:197], v[10:13]
	v_mfma_f32_16x16x32_bf16 v[34:37], v[210:213], v[190:193], v[34:37]
	v_mfma_f32_16x16x32_bf16 v[2:5], v[210:213], v[194:197], v[2:5]
	ds_read_b128 v[164:167], v214 offset:38912
	ds_read_b128 v[190:193], v214 offset:40960
	ds_read_b128 v[194:197], v214 offset:43008
	ds_read_b128 v[198:201], v215 offset:16384
	ds_read_b128 v[202:205], v215 offset:18432
	ds_read_b128 v[206:209], v215 offset:20480
	ds_read_b128 v[210:213], v215 offset:22528
	s_waitcnt lgkmcnt(3)
; #define LAS __attribute__((address_space(3)))
; #define MS_WLOAD(set, t) do { _Pragma("unroll") for (int r_ = 0; r_ < 4; ++r_) wr[set][r_] = __builtin_bit_cast(f32x4, __builtin_amdgcn_raw_buffer_load_b128(wrs, (int)wvo + r_ * LDW * 4, MS_CL(t) * (64 * LDW * 4), 0)); } while (0)
; #define MS_WCOMMIT(set, bufi) do { LAS unsigned char* wb_ = lds + (bufi) * MS_TILE; _Pragma("unroll") for (int i_ = 0; i_ < 4; ++i_) { \
;             u32x2 p_; p_.x = pk2(wr[set][0][i_], wr[set][1][i_]); p_.y = pk2(wr[set][2][i_], wr[set][3][i_]); \
;             *(LAS u32x2*)(wb_ + ((i_ < 2) ? lw0 : lw1) + i_ * 128) = p_; } } while (0)
; #define MS_XSLOAD(t) do { _Pragma("unroll") for (int i_ = 0; i_ < 6; ++i_) xs[i_] = __builtin_bit_cast(bf16x8, __builtin_amdgcn_raw_buffer_load_b128(xrs, (int)xso[i_], MS_CL(t) * 128, 0)); } while (0)
; #define MS_XSWRITE(bufi) do { _Pragma("unroll") for (int i_ = 0; i_ < 6; ++i_) *(LAS bf16x8*)(xw + (bufi) * MS_XBUF + i_ * 1024 + ((i_ & 1) ? (xwo ^ 64) : xwo)) = xs[i_]; } while (0)
; #define MS_STEP(I, J, t) do { MS_WCOMMIT(J, J); MS_WLOAD(J, (t) + 3); MS_COMPUTE(I); MS_XSWRITE(J); MS_XSLOAD((t) + 2); __syncthreads(); } while (0)
;     ...
;             const LAS unsigned char* xr1 = lds + MS_XOFF + wave * MS_XWAVE + tk * 128 + (((4 + q) ^ rd_g) << 4);
;             __syncthreads();
;             MS_XSLOAD(0); MS_WLOAD(0, 0); MS_WLOAD(1, 1);
;             MS_WCOMMIT(0, 0); MS_WLOAD(0, 2);
;             MS_XSWRITE(0); MS_XSLOAD(1);
;             __syncthreads();
; #pragma unroll 1
;             for (int t = 0; t < NT; t += 2) { MS_STEP(0, 1, t); MS_STEP(1, 0, t + 1); }
	v_mfma_f32_16x16x32_bf16 v[152:155], v[198:201], v[164:167], v[152:155]
	v_mfma_f32_16x16x32_bf16 v[62:65], v[198:201], v[190:193], v[62:65]
	v_mfma_f32_16x16x32_bf16 v[30:33], v[198:201], v[194:197], v[30:33]
	s_waitcnt lgkmcnt(2)
	v_mfma_f32_16x16x32_bf16 v[120:123], v[202:205], v[164:167], v[120:123]
	v_mfma_f32_16x16x32_bf16 v[54:57], v[202:205], v[190:193], v[54:57]
	v_mfma_f32_16x16x32_bf16 v[22:25], v[202:205], v[194:197], v[22:25]
	s_waitcnt lgkmcnt(1)
	v_mfma_f32_16x16x32_bf16 v[112:115], v[206:209], v[164:167], v[112:115]
	v_mfma_f32_16x16x32_bf16 v[46:49], v[206:209], v[190:193], v[46:49]
	v_mfma_f32_16x16x32_bf16 v[14:17], v[206:209], v[194:197], v[14:17]
	s_waitcnt lgkmcnt(0)
	v_mfma_f32_16x16x32_bf16 v[70:73], v[210:213], v[164:167], v[70:73]
	v_mfma_f32_16x16x32_bf16 v[38:41], v[210:213], v[190:193], v[38:41]
	v_mfma_f32_16x16x32_bf16 v[6:9], v[210:213], v[194:197], v[6:9]
	ds_read_b128 v[198:201], v215 offset:24576
	ds_read_b128 v[202:205], v215 offset:26624
	ds_read_b128 v[206:209], v215 offset:28672
	ds_read_b128 v[210:213], v215 offset:30720
	s_waitcnt lgkmcnt(3)
	v_mfma_f32_16x16x32_bf16 v[148:151], v[198:201], v[164:167], v[148:151]
	v_mfma_f32_16x16x32_bf16 v[58:61], v[198:201], v[190:193], v[58:61]
	v_mfma_f32_16x16x32_bf16 v[26:29], v[198:201], v[194:197], v[26:29]
	s_waitcnt lgkmcnt(2)
	v_mfma_f32_16x16x32_bf16 v[116:119], v[202:205], v[164:167], v[116:119]
	v_mfma_f32_16x16x32_bf16 v[50:53], v[202:205], v[190:193], v[50:53]
	v_mfma_f32_16x16x32_bf16 v[18:21], v[202:205], v[194:197], v[18:21]
	s_waitcnt lgkmcnt(1)
	v_mfma_f32_16x16x32_bf16 v[92:95], v[206:209], v[164:167], v[92:95]
	v_mfma_f32_16x16x32_bf16 v[42:45], v[206:209], v[190:193], v[42:45]
	v_mfma_f32_16x16x32_bf16 v[10:13], v[206:209], v[194:197], v[10:13]
	s_waitcnt lgkmcnt(0)
	v_mfma_f32_16x16x32_bf16 v[66:69], v[210:213], v[164:167], v[66:69]
	v_mfma_f32_16x16x32_bf16 v[34:37], v[210:213], v[190:193], v[34:37]
	v_mfma_f32_16x16x32_bf16 v[2:5], v[210:213], v[194:197], v[2:5]
	ds_read_b128 v[164:167], v216 offset:38912
	ds_read_b128 v[190:193], v216 offset:40960
	ds_read_b128 v[194:197], v216 offset:43008
	ds_read_b128 v[198:201], v217 offset:16384
	ds_read_b128 v[202:205], v217 offset:18432
	ds_read_b128 v[206:209], v217 offset:20480
	ds_read_b128 v[210:213], v217 offset:22528
	s_waitcnt lgkmcnt(3)
	v_mfma_f32_16x16x32_bf16 v[152:155], v[198:201], v[164:167], v[152:155]
	v_mfma_f32_16x16x32_bf16 v[62:65], v[198:201], v[190:193], v[62:65]
	v_mfma_f32_16x16x32_bf16 v[30:33], v[198:201], v[194:197], v[30:33]
	s_waitcnt lgkmcnt(2)
	v_mfma_f32_16x16x32_bf16 v[120:123], v[202:205], v[164:167], v[120:123]
	v_mfma_f32_16x16x32_bf16 v[54:57], v[202:205], v[190:193], v[54:57]
	v_mfma_f32_16x16x32_bf16 v[22:25], v[202:205], v[194:197], v[22:25]
	s_waitcnt lgkmcnt(1)
	v_mfma_f32_16x16x32_bf16 v[112:115], v[206:209], v[164:167], v[112:115]
	v_mfma_f32_16x16x32_bf16 v[46:49], v[206:209], v[190:193], v[46:49]
	v_mfma_f32_16x16x32_bf16 v[14:17], v[206:209], v[194:197], v[14:17]
	s_waitcnt lgkmcnt(0)
	v_mfma_f32_16x16x32_bf16 v[70:73], v[210:213], v[164:167], v[70:73]
	v_mfma_f32_16x16x32_bf16 v[38:41], v[210:213], v[190:193], v[38:41]
	v_mfma_f32_16x16x32_bf16 v[6:9], v[210:213], v[194:197], v[6:9]
	ds_read_b128 v[198:201], v217 offset:24576
	ds_read_b128 v[202:205], v217 offset:26624
	ds_read_b128 v[206:209], v217 offset:28672
	ds_read_b128 v[210:213], v217 offset:30720
	s_lshl_b32 s1, s1, 7
	s_waitcnt vmcnt(9)
	ds_write_b128 v189, v[124:127] offset:32768
	s_waitcnt vmcnt(8)
	ds_write_b128 v181, v[128:131] offset:33792
	s_waitcnt vmcnt(7)
	ds_write_b128 v189, v[132:135] offset:34816
	s_waitcnt vmcnt(6)
	ds_write_b128 v181, v[136:139] offset:35840
	s_waitcnt vmcnt(5)
	ds_write_b128 v189, v[140:143] offset:36864
	s_waitcnt vmcnt(4)
	ds_write_b128 v181, v[144:147] offset:37888
	s_addk_i32 s1, 0x180
	s_cmp_eq_u32 s0, 30
	s_cselect_b32 s58, s84, 0
	s_cmp_lg_u32 s58, 0
	s_cselect_b32 s1, 0x80, s1
	buffer_load_dwordx4 v[132:135], v182, s[4:7], s1 offen
	buffer_load_dwordx4 v[124:127], v183, s[4:7], s1 offen
	buffer_load_dwordx4 v[140:143], v184, s[4:7], s1 offen
	buffer_load_dwordx4 v[144:147], v185, s[4:7], s1 offen
	buffer_load_dwordx4 v[128:131], v186, s[4:7], s1 offen
	buffer_load_dwordx4 v[136:139], v187, s[4:7], s1 offen
	s_waitcnt lgkmcnt(9)
	v_mfma_f32_16x16x32_bf16 v[148:151], v[198:201], v[164:167], v[148:151]
	s_cmp_gt_u32 s0, 29
	s_waitcnt lgkmcnt(0)
	s_barrier
	v_mfma_f32_16x16x32_bf16 v[58:61], v[198:201], v[190:193], v[58:61]
	v_mfma_f32_16x16x32_bf16 v[26:29], v[198:201], v[194:197], v[26:29]
	v_mfma_f32_16x16x32_bf16 v[116:119], v[202:205], v[164:167], v[116:119]
	v_mfma_f32_16x16x32_bf16 v[50:53], v[202:205], v[190:193], v[50:53]
	v_mfma_f32_16x16x32_bf16 v[18:21], v[202:205], v[194:197], v[18:21]
	v_mfma_f32_16x16x32_bf16 v[92:95], v[206:209], v[164:167], v[92:95]
	v_mfma_f32_16x16x32_bf16 v[42:45], v[206:209], v[190:193], v[42:45]
	v_mfma_f32_16x16x32_bf16 v[10:13], v[206:209], v[194:197], v[10:13]
	v_mfma_f32_16x16x32_bf16 v[66:69], v[210:213], v[164:167], v[66:69]
	v_mfma_f32_16x16x32_bf16 v[34:37], v[210:213], v[190:193], v[34:37]
	v_mfma_f32_16x16x32_bf16 v[2:5], v[210:213], v[194:197], v[2:5]
	s_cbranch_scc0 .LBB0_1720
	s_branch .Lmoe_k_done
; #define LAS __attribute__((address_space(3)))
; #define MS_WLOAD(set, t) do { _Pragma("unroll") for (int r_ = 0; r_ < 4; ++r_) wr[set][r_] = __builtin_bit_cast(f32x4, __builtin_amdgcn_raw_buffer_load_b128(wrs, (int)wvo + r_ * LDW * 4, MS_CL(t) * (64 * LDW * 4), 0)); } while (0)
; #define MS_WCOMMIT(set, bufi) do { LAS unsigned char* wb_ = lds + (bufi) * MS_TILE; _Pragma("unroll") for (int i_ = 0; i_ < 4; ++i_) { \
;             u32x2 p_; p_.x = pk2(wr[set][0][i_], wr[set][1][i_]); p_.y = pk2(wr[set][2][i_], wr[set][3][i_]); \
;             *(LAS u32x2*)(wb_ + ((i_ < 2) ? lw0 : lw1) + i_ * 128) = p_; } } while (0)
; #define MS_XSLOAD(t) do { _Pragma("unroll") for (int i_ = 0; i_ < 6; ++i_) xs[i_] = __builtin_bit_cast(bf16x8, __builtin_amdgcn_raw_buffer_load_b128(xrs, (int)xso[i_], MS_CL(t) * 128, 0)); } while (0)
; #define MS_XSWRITE(bufi) do { _Pragma("unroll") for (int i_ = 0; i_ < 6; ++i_) *(LAS bf16x8*)(xw + (bufi) * MS_XBUF + i_ * 1024 + ((i_ & 1) ? (xwo ^ 64) : xwo)) = xs[i_]; } while (0)
; #define MS_STEP(I, J, t) do { MS_WCOMMIT(J, J); MS_WLOAD(J, (t) + 3); MS_COMPUTE(I); MS_XSWRITE(J); MS_XSLOAD((t) + 2); __syncthreads(); } while (0)
;     ...
;             const LAS unsigned char* xr1 = lds + MS_XOFF + wave * MS_XWAVE + tk * 128 + (((4 + q) ^ rd_g) << 4);
;             __syncthreads();
;             MS_XSLOAD(0); MS_WLOAD(0, 0); MS_WLOAD(1, 1);
;             MS_WCOMMIT(0, 0); MS_WLOAD(0, 2);
;             MS_XSWRITE(0); MS_XSLOAD(1);
;             __syncthreads();
; #pragma unroll 1
;             for (int t = 0; t < NT; t += 2) { MS_STEP(0, 1, t); MS_STEP(1, 0, t + 1); }
.Lmoe_k_b:
	s_add_i32 s0, s0, 2
	s_min_u32 s1, s0, 28
	s_lshl_b32 s12, s1, 17
	s_add_i32 s12, s12, 0x60000
	s_add_i32 s58, s85, 0x20000
	s_cmp_gt_u32 s0, 28
	s_cselect_b32 s12, s58, s12
	s_waitcnt vmcnt(12)
	v_cvt_pk_bf16_f32 v164, v74, v78
	s_waitcnt vmcnt(10)
	v_cvt_pk_bf16_f32 v165, v82, v86
	v_cvt_pk_bf16_f32 v166, v75, v79
	v_cvt_pk_bf16_f32 v167, v83, v87
	v_cvt_pk_bf16_f32 v190, v76, v80
	v_cvt_pk_bf16_f32 v191, v84, v88
	v_cvt_pk_bf16_f32 v192, v77, v81
	v_cvt_pk_bf16_f32 v193, v85, v89
	buffer_load_dwordx4 v[74:77], v160, s[8:11], s12 offen nt
	buffer_load_dwordx4 v[78:81], v90, s[8:11], s12 offen nt
	buffer_load_dwordx4 v[82:85], v178, s[8:11], s12 offen nt
	buffer_load_dwordx4 v[86:89], v179, s[8:11], s12 offen nt
	v_add_u32_e32 v194, 0x4000, v188
	v_add_u32_e32 v195, 0x4000, v180
	v_add_u32_e32 v214, v173, v174
	ds_write2_b64 v194, v[164:165], v[166:167] offset1:16
	ds_write2_b64 v195, v[190:191], v[192:193] offset0:32 offset1:48
	v_add_u32_e32 v215, v176, v174
	ds_read_b128 v[164:167], v214 offset:32768
	ds_read_b128 v[190:193], v214 offset:34816
	ds_read_b128 v[198:201], v215
	ds_read_b128 v[202:205], v215 offset:2048
	ds_read_b128 v[206:209], v215 offset:4096
	ds_read_b128 v[210:213], v215 offset:6144
	s_waitcnt lgkmcnt(3)
	v_mfma_f32_16x16x32_bf16 v[152:155], v[198:201], v[164:167], v[152:155]
	v_mfma_f32_16x16x32_bf16 v[62:65], v[198:201], v[190:193], v[62:65]
	s_waitcnt lgkmcnt(2)
	v_mfma_f32_16x16x32_bf16 v[120:123], v[202:205], v[164:167], v[120:123]
	v_mfma_f32_16x16x32_bf16 v[54:57], v[202:205], v[190:193], v[54:57]
	s_waitcnt lgkmcnt(1)
	v_mfma_f32_16x16x32_bf16 v[112:115], v[206:209], v[164:167], v[112:115]
	v_mfma_f32_16x16x32_bf16 v[46:49], v[206:209], v[190:193], v[46:49]
	s_waitcnt lgkmcnt(0)
	v_mfma_f32_16x16x32_bf16 v[70:73], v[210:213], v[164:167], v[70:73]
	v_mfma_f32_16x16x32_bf16 v[38:41], v[210:213], v[190:193], v[38:41]
	ds_read_b128 v[198:201], v215 offset:8192
	ds_read_b128 v[202:205], v215 offset:10240
	ds_read_b128 v[206:209], v215 offset:12288
	ds_read_b128 v[210:213], v215 offset:14336
	s_waitcnt lgkmcnt(3)
	v_mfma_f32_16x16x32_bf16 v[148:151], v[198:201], v[164:167], v[148:151]
	v_mfma_f32_16x16x32_bf16 v[58:61], v[198:201], v[190:193], v[58:61]
	s_waitcnt lgkmcnt(2)
	v_mfma_f32_16x16x32_bf16 v[116:119], v[202:205], v[164:167], v[116:119]
	v_mfma_f32_16x16x32_bf16 v[50:53], v[202:205], v[190:193], v[50:53]
	s_waitcnt lgkmcnt(1)
	v_mfma_f32_16x16x32_bf16 v[92:95], v[206:209], v[164:167], v[92:95]
	v_mfma_f32_16x16x32_bf16 v[42:45], v[206:209], v[190:193], v[42:45]
	s_waitcnt lgkmcnt(0)
	v_mfma_f32_16x16x32_bf16 v[66:69], v[210:213], v[164:167], v[66:69]
	v_mfma_f32_16x16x32_bf16 v[34:37], v[210:213], v[190:193], v[34:37]
	v_add_u32_e32 v216, v173, v175
	ds_read_b128 v[164:167], v216 offset:32768
	ds_read_b128 v[190:193], v216 offset:34816
	v_add_u32_e32 v217, v176, v175
	ds_read_b128 v[198:201], v217
	ds_read_b128 v[202:205], v217 offset:2048
	ds_read_b128 v[206:209], v217 offset:4096
	ds_read_b128 v[210:213], v217 offset:6144
	s_waitcnt lgkmcnt(3)
	v_mfma_f32_16x16x32_bf16 v[152:155], v[198:201], v[164:167], v[152:155]
	v_mfma_f32_16x16x32_bf16 v[62:65], v[198:201], v[190:193], v[62:65]
	s_waitcnt lgkmcnt(2)
	v_mfma_f32_16x16x32_bf16 v[120:123], v[202:205], v[164:167], v[120:123]
	v_mfma_f32_16x16x32_bf16 v[54:57], v[202:205], v[190:193], v[54:57]
	s_waitcnt lgkmcnt(1)
	v_mfma_f32_16x16x32_bf16 v[112:115], v[206:209], v[164:167], v[112:115]
	v_mfma_f32_16x16x32_bf16 v[46:49], v[206:209], v[190:193], v[46:49]
	s_waitcnt lgkmcnt(0)
	v_mfma_f32_16x16x32_bf16 v[70:73], v[210:213], v[164:167], v[70:73]
	v_mfma_f32_16x16x32_bf16 v[38:41], v[210:213], v[190:193], v[38:41]
	ds_read_b128 v[198:201], v217 offset:8192
	ds_read_b128 v[202:205], v217 offset:10240
	ds_read_b128 v[206:209], v217 offset:12288
	ds_read_b128 v[210:213], v217 offset:14336
	s_min_u32 s12, s0, 29
	s_lshl_b32 s12, s12, 7
	s_waitcnt vmcnt(7)
	ds_write_b128 v189, v[132:135] offset:38912
	s_waitcnt vmcnt(6)
	ds_write_b128 v181, v[124:127] offset:39936
	s_waitcnt vmcnt(5)
	ds_write_b128 v189, v[140:143] offset:40960
	s_waitcnt vmcnt(4)
	ds_write_b128 v181, v[144:147] offset:41984
	s_addk_i32 s12, 0x100
	s_cmp_lt_u32 s0, 30
	s_cbranch_scc1 .Lxk_nx1
	s_cmp_eq_u32 s84, 0
	s_cbranch_scc1 .Lxk_nx1
	s_mov_b32 s12, 0
	v_lshl_or_b32 v182, v246, 12, v163
	v_lshl_or_b32 v183, v247, 12, v163
	v_lshl_or_b32 v184, v248, 12, v163
	v_lshl_or_b32 v185, v249, 12, v163
	v_lshl_or_b32 v186, v250, 12, v163
	v_lshl_or_b32 v187, v251, 12, v163
; #define LAS __attribute__((address_space(3)))
; #define MS_WLOAD(set, t) do { _Pragma("unroll") for (int r_ = 0; r_ < 4; ++r_) wr[set][r_] = __builtin_bit_cast(f32x4, __builtin_amdgcn_raw_buffer_load_b128(wrs, (int)wvo + r_ * LDW * 4, MS_CL(t) * (64 * LDW * 4), 0)); } while (0)
; #define MS_WCOMMIT(set, bufi) do { LAS unsigned char* wb_ = lds + (bufi) * MS_TILE; _Pragma("unroll") for (int i_ = 0; i_ < 4; ++i_) { \
;             u32x2 p_; p_.x = pk2(wr[set][0][i_], wr[set][1][i_]); p_.y = pk2(wr[set][2][i_], wr[set][3][i_]); \
;             *(LAS u32x2*)(wb_ + ((i_ < 2) ? lw0 : lw1) + i_ * 128) = p_; } } while (0)
; #define MS_XSLOAD(t) do { _Pragma("unroll") for (int i_ = 0; i_ < 6; ++i_) xs[i_] = __builtin_bit_cast(bf16x8, __builtin_amdgcn_raw_buffer_load_b128(xrs, (int)xso[i_], MS_CL(t) * 128, 0)); } while (0)
; #define MS_XSWRITE(bufi) do { _Pragma("unroll") for (int i_ = 0; i_ < 6; ++i_) *(LAS bf16x8*)(xw + (bufi) * MS_XBUF + i_ * 1024 + ((i_ & 1) ? (xwo ^ 64) : xwo)) = xs[i_]; } while (0)
; #define MS_STEP(I, J, t) do { MS_WCOMMIT(J, J); MS_WLOAD(J, (t) + 3); MS_COMPUTE(I); MS_XSWRITE(J); MS_XSLOAD((t) + 2); __syncthreads(); } while (0)
;     ...
;             const LAS unsigned char* xr1 = lds + MS_XOFF + wave * MS_XWAVE + tk * 128 + (((4 + q) ^ rd_g) << 4);
;             __syncthreads();
;             MS_XSLOAD(0); MS_WLOAD(0, 0); MS_WLOAD(1, 1);
;             MS_WCOMMIT(0, 0); MS_WLOAD(0, 2);
;             MS_XSWRITE(0); MS_XSLOAD(1);
;             __syncthreads();
; #pragma unroll 1
;             for (int t = 0; t < NT; t += 2) { MS_STEP(0, 1, t); MS_STEP(1, 0, t + 1); }
.Lxk_nx1:
	s_waitcnt lgkmcnt(7)
	v_mfma_f32_16x16x32_bf16 v[148:151], v[198:201], v[164:167], v[148:151]
	buffer_load_dwordx4 v[124:127], v182, s[4:7], s12 offen
	buffer_load_dwordx4 v[128:131], v183, s[4:7], s12 offen
	buffer_load_dwordx4 v[132:135], v184, s[4:7], s12 offen
	buffer_load_dwordx4 v[136:139], v185, s[4:7], s12 offen
	s_min_u32 s12, s0, 27
	s_waitcnt lgkmcnt(0)
	v_mfma_f32_16x16x32_bf16 v[116:119], v[202:205], v[164:167], v[116:119]
	s_barrier
	s_lshl_b32 s12, s12, 17
	v_mfma_f32_16x16x32_bf16 v[92:95], v[206:209], v[164:167], v[92:95]
	s_add_i32 s12, s12, 0x80000
	s_sub_i32 s58, s0, 28
	s_lshl_b32 s58, s58, 17
	s_add_i32 s58, s58, s85
	s_cmp_gt_u32 s0, 27
	s_cselect_b32 s12, s58, s12
	v_mfma_f32_16x16x32_bf16 v[66:69], v[210:213], v[164:167], v[66:69]
	v_cvt_pk_bf16_f32 v164, v96, v100
	v_cvt_pk_bf16_f32 v165, v104, v108
	v_cvt_pk_bf16_f32 v96, v97, v101
	v_cvt_pk_bf16_f32 v97, v105, v109
	ds_write2_b64 v188, v[164:165], v[96:97] offset1:16
	v_cvt_pk_bf16_f32 v96, v98, v102
	v_cvt_pk_bf16_f32 v97, v106, v110
	v_cvt_pk_bf16_f32 v98, v99, v103
	v_cvt_pk_bf16_f32 v99, v107, v111
	ds_write2_b64 v180, v[96:97], v[98:99] offset0:32 offset1:48
	buffer_load_dwordx4 v[96:99], v160, s[8:11], s12 offen nt
	buffer_load_dwordx4 v[100:103], v90, s[8:11], s12 offen nt
	buffer_load_dwordx4 v[104:107], v178, s[8:11], s12 offen nt
	buffer_load_dwordx4 v[108:111], v179, s[8:11], s12 offen nt
	v_mfma_f32_16x16x32_bf16 v[58:61], v[198:201], v[190:193], v[58:61]
	v_mfma_f32_16x16x32_bf16 v[50:53], v[202:205], v[190:193], v[50:53]
	v_mfma_f32_16x16x32_bf16 v[42:45], v[206:209], v[190:193], v[42:45]
	v_mfma_f32_16x16x32_bf16 v[34:37], v[210:213], v[190:193], v[34:37]
	ds_read_b128 v[164:167], v214 offset:38912
	ds_read_b128 v[190:193], v214 offset:40960
	ds_read_b128 v[198:201], v215 offset:16384
	ds_read_b128 v[202:205], v215 offset:18432
	ds_read_b128 v[206:209], v215 offset:20480
	ds_read_b128 v[210:213], v215 offset:22528
	s_waitcnt lgkmcnt(3)
	v_mfma_f32_16x16x32_bf16 v[152:155], v[198:201], v[164:167], v[152:155]
	v_mfma_f32_16x16x32_bf16 v[62:65], v[198:201], v[190:193], v[62:65]
	s_waitcnt lgkmcnt(2)
	v_mfma_f32_16x16x32_bf16 v[120:123], v[202:205], v[164:167], v[120:123]
	v_mfma_f32_16x16x32_bf16 v[54:57], v[202:205], v[190:193], v[54:57]
	s_waitcnt lgkmcnt(1)
	v_mfma_f32_16x16x32_bf16 v[112:115], v[206:209], v[164:167], v[112:115]
	v_mfma_f32_16x16x32_bf16 v[46:49], v[206:209], v[190:193], v[46:49]
	s_waitcnt lgkmcnt(0)
	v_mfma_f32_16x16x32_bf16 v[70:73], v[210:213], v[164:167], v[70:73]
	v_mfma_f32_16x16x32_bf16 v[38:41], v[210:213], v[190:193], v[38:41]
	ds_read_b128 v[198:201], v215 offset:24576
	ds_read_b128 v[202:205], v215 offset:26624
	ds_read_b128 v[206:209], v215 offset:28672
	ds_read_b128 v[210:213], v215 offset:30720
	s_waitcnt lgkmcnt(3)
	v_mfma_f32_16x16x32_bf16 v[148:151], v[198:201], v[164:167], v[148:151]
	v_mfma_f32_16x16x32_bf16 v[58:61], v[198:201], v[190:193], v[58:61]
	s_waitcnt lgkmcnt(2)
	v_mfma_f32_16x16x32_bf16 v[116:119], v[202:205], v[164:167], v[116:119]
	v_mfma_f32_16x16x32_bf16 v[50:53], v[202:205], v[190:193], v[50:53]
	s_waitcnt lgkmcnt(1)
	v_mfma_f32_16x16x32_bf16 v[92:95], v[206:209], v[164:167], v[92:95]
	v_mfma_f32_16x16x32_bf16 v[42:45], v[206:209], v[190:193], v[42:45]
	s_waitcnt lgkmcnt(0)
	v_mfma_f32_16x16x32_bf16 v[66:69], v[210:213], v[164:167], v[66:69]
	v_mfma_f32_16x16x32_bf16 v[34:37], v[210:213], v[190:193], v[34:37]
	ds_read_b128 v[164:167], v216 offset:38912
	ds_read_b128 v[190:193], v216 offset:40960
	ds_read_b128 v[198:201], v217 offset:16384
	ds_read_b128 v[202:205], v217 offset:18432
	ds_read_b128 v[206:209], v217 offset:20480
	ds_read_b128 v[210:213], v217 offset:22528
	s_waitcnt lgkmcnt(3)
	v_mfma_f32_16x16x32_bf16 v[152:155], v[198:201], v[164:167], v[152:155]
	v_mfma_f32_16x16x32_bf16 v[62:65], v[198:201], v[190:193], v[62:65]
	s_waitcnt lgkmcnt(2)
	v_mfma_f32_16x16x32_bf16 v[120:123], v[202:205], v[164:167], v[120:123]
	v_mfma_f32_16x16x32_bf16 v[54:57], v[202:205], v[190:193], v[54:57]
	s_waitcnt lgkmcnt(1)
	v_mfma_f32_16x16x32_bf16 v[112:115], v[206:209], v[164:167], v[112:115]
	v_mfma_f32_16x16x32_bf16 v[46:49], v[206:209], v[190:193], v[46:49]
	s_waitcnt lgkmcnt(0)
	v_mfma_f32_16x16x32_bf16 v[70:73], v[210:213], v[164:167], v[70:73]
	v_mfma_f32_16x16x32_bf16 v[38:41], v[210:213], v[190:193], v[38:41]
	ds_read_b128 v[198:201], v217 offset:24576
	ds_read_b128 v[202:205], v217 offset:26624
	ds_read_b128 v[206:209], v217 offset:28672
	ds_read_b128 v[210:213], v217 offset:30720
	s_lshl_b32 s1, s1, 7
	s_waitcnt vmcnt(7)
	ds_write_b128 v189, v[124:127] offset:32768
	s_waitcnt vmcnt(6)
	ds_write_b128 v181, v[128:131] offset:33792
	s_waitcnt vmcnt(5)
	ds_write_b128 v189, v[132:135] offset:34816
	s_waitcnt vmcnt(4)
	ds_write_b128 v181, v[136:139] offset:35840
	s_addk_i32 s1, 0x180
	s_cmp_eq_u32 s0, 30
	s_cselect_b32 s58, s84, 0
	s_cmp_lg_u32 s58, 0
	s_cselect_b32 s1, 0x80, s1
	buffer_load_dwordx4 v[132:135], v182, s[4:7], s1 offen
	buffer_load_dwordx4 v[124:127], v183, s[4:7], s1 offen
	buffer_load_dwordx4 v[140:143], v184, s[4:7], s1 offen
	buffer_load_dwordx4 v[144:147], v185, s[4:7], s1 offen
	s_waitcnt lgkmcnt(7)
	v_mfma_f32_16x16x32_bf16 v[148:151], v[198:201], v[164:167], v[148:151]
	s_cmp_gt_u32 s0, 29
	s_waitcnt lgkmcnt(0)
	s_barrier
	v_mfma_f32_16x16x32_bf16 v[58:61], v[198:201], v[190:193], v[58:61]
	v_mfma_f32_16x16x32_bf16 v[116:119], v[202:205], v[164:167], v[116:119]
	v_mfma_f32_16x16x32_bf16 v[50:53], v[202:205], v[190:193], v[50:53]
	v_mfma_f32_16x16x32_bf16 v[92:95], v[206:209], v[164:167], v[92:95]
	v_mfma_f32_16x16x32_bf16 v[42:45], v[206:209], v[190:193], v[42:45]
	v_mfma_f32_16x16x32_bf16 v[66:69], v[210:213], v[164:167], v[66:69]
	v_mfma_f32_16x16x32_bf16 v[34:37], v[210:213], v[190:193], v[34:37]
	s_cbranch_scc0 .Lmoe_k_b
; DI unsigned pk2(float a, float b) { f32x2 v = {a, b}; bf16x2_t r = __builtin_convertvector(v, bf16x2_t); return __builtin_bit_cast(unsigned, r); }
; DI float sigmoidf_(float x) { return 1.f / (1.f + __expf(-x)); }
;     ...
; #pragma unroll
;             for (int mt = 0; mt < 3; ++mt) { const int tok = rp + wave * 48 + mt * 16 + tk;
;                 if (tok < M) {
;                     if (MODE == 0) { bf16* o = (bf16*)(ws + o_hid) + (size_t)(row0 + tok) * DEXP + slab * 64 + 4 * q;
; #pragma unroll
;                         for (int j = 0; j < 4; ++j) { float h[4];
; #pragma unroll
;                             for (int i = 0; i < 4; ++i) { const float gt = acc[mt][j][i]; h[i] = gt * sigmoidf_(gt) * acc[mt][j + 4][i]; }
;                             *(u32x2*)(o + 16 * j) = (u32x2){pk2(h[0], h[1]), pk2(h[2], h[3])}; }
.Lmoe_k_done:
	v_add_u32_e32 v236, s31, v177
	v_cmp_gt_i32_e32 vcc, s28, v236
	s_and_saveexec_b64 s[12:13], vcc
	s_cbranch_execz .LBB0_1723
	v_mul_f32_e32 v237, 0xbfb8aa3b, v152
	v_exp_f32_e32 v238, v237
	v_mul_f32_e32 v237, 0xbfb8aa3b, v153
	v_exp_f32_e32 v239, v237
	v_add_u32_e32 v234, s29, v236
	v_ashrrev_i32_e32 v235, 31, v234
	v_lshlrev_b64 v[234:235], 10, v[234:235]
	v_pk_add_f32 v[238:239], v[238:239], 1.0 op_sel_hi:[1,0]
	v_lshl_add_u64 v[234:235], v[158:159], 0, v[234:235]
	v_rcp_f32_e32 v239, v239
	v_rcp_f32_e32 v238, v238
	v_mul_f32_e32 v237, 0xbfb8aa3b, v154
	v_exp_f32_e32 v240, v237
	v_mul_f32_e32 v237, 0xbfb8aa3b, v155
	v_exp_f32_e32 v241, v237
	v_pk_mul_f32 v[238:239], v[152:153], v[238:239]
	v_pk_add_f32 v[240:241], v[240:241], 1.0 op_sel_hi:[1,0]
	s_nop 0
	v_pk_mul_f32 v[238:239], v[238:239], v[148:149]
	v_rcp_f32_e32 v241, v241
	v_cvt_pk_bf16_f32 v238, v238, v239
	v_rcp_f32_e32 v240, v240
	s_nop 0
	v_pk_mul_f32 v[240:241], v[154:155], v[240:241]
	v_mul_f32_e32 v237, 0xbfb8aa3b, v120
	v_pk_mul_f32 v[240:241], v[240:241], v[150:151]
	s_nop 0
	v_cvt_pk_bf16_f32 v239, v240, v241
	global_store_dwordx2 v[234:235], v[238:239], off
	v_exp_f32_e32 v238, v237
	v_mul_f32_e32 v237, 0xbfb8aa3b, v121
	v_exp_f32_e32 v239, v237
	s_nop 0
	v_pk_add_f32 v[238:239], v[238:239], 1.0 op_sel_hi:[1,0]
	s_nop 0
	v_rcp_f32_e32 v239, v239
	v_rcp_f32_e32 v238, v238
	v_mul_f32_e32 v237, 0xbfb8aa3b, v122
	v_exp_f32_e32 v240, v237
	v_mul_f32_e32 v237, 0xbfb8aa3b, v123
	v_exp_f32_e32 v241, v237
	v_pk_mul_f32 v[238:239], v[120:121], v[238:239]
	v_pk_add_f32 v[240:241], v[240:241], 1.0 op_sel_hi:[1,0]
	s_nop 0
	v_pk_mul_f32 v[238:239], v[238:239], v[116:117]
	v_rcp_f32_e32 v241, v241
	v_cvt_pk_bf16_f32 v238, v238, v239
	v_rcp_f32_e32 v240, v240
	s_nop 0
	v_pk_mul_f32 v[240:241], v[122:123], v[240:241]
	v_mul_f32_e32 v237, 0xbfb8aa3b, v112
	v_pk_mul_f32 v[240:241], v[240:241], v[118:119]
	s_nop 0
	v_cvt_pk_bf16_f32 v239, v240, v241
	global_store_dwordx2 v[234:235], v[238:239], off offset:32
	v_exp_f32_e32 v238, v237
	v_mul_f32_e32 v237, 0xbfb8aa3b, v113
	v_exp_f32_e32 v239, v237
	s_nop 0
	v_pk_add_f32 v[238:239], v[238:239], 1.0 op_sel_hi:[1,0]
	s_nop 0
	v_rcp_f32_e32 v239, v239
	v_rcp_f32_e32 v238, v238
	v_mul_f32_e32 v237, 0xbfb8aa3b, v114
	v_exp_f32_e32 v240, v237
	v_mul_f32_e32 v237, 0xbfb8aa3b, v115
	v_exp_f32_e32 v241, v237
	v_pk_mul_f32 v[238:239], v[112:113], v[238:239]
	v_pk_add_f32 v[240:241], v[240:241], 1.0 op_sel_hi:[1,0]
	s_nop 0
	v_pk_mul_f32 v[238:239], v[238:239], v[92:93]
	v_rcp_f32_e32 v241, v241
	v_cvt_pk_bf16_f32 v238, v238, v239
	v_rcp_f32_e32 v240, v240
	s_nop 0
	v_pk_mul_f32 v[240:241], v[114:115], v[240:241]
	v_mul_f32_e32 v237, 0xbfb8aa3b, v70
	v_pk_mul_f32 v[240:241], v[240:241], v[94:95]
	s_nop 0
	v_cvt_pk_bf16_f32 v239, v240, v241
	global_store_dwordx2 v[234:235], v[238:239], off offset:64
	v_exp_f32_e32 v238, v237
	v_mul_f32_e32 v237, 0xbfb8aa3b, v71
	v_exp_f32_e32 v239, v237
	s_nop 0
	v_pk_add_f32 v[238:239], v[238:239], 1.0 op_sel_hi:[1,0]
	s_nop 0
	v_rcp_f32_e32 v239, v239
	v_rcp_f32_e32 v238, v238
	s_nop 0
	v_pk_mul_f32 v[70:71], v[70:71], v[238:239]
	s_nop 0
	v_pk_mul_f32 v[66:67], v[70:71], v[66:67]
	v_mul_f32_e32 v70, 0xbfb8aa3b, v72
	v_mul_f32_e32 v71, 0xbfb8aa3b, v73
	v_exp_f32_e32 v70, v70
	v_exp_f32_e32 v71, v71
	v_cvt_pk_bf16_f32 v66, v66, v67
	v_pk_add_f32 v[70:71], v[70:71], 1.0 op_sel_hi:[1,0]
	s_nop 0
	v_rcp_f32_e32 v71, v71
	v_rcp_f32_e32 v70, v70
	s_nop 0
	v_pk_mul_f32 v[70:71], v[72:73], v[70:71]
	s_nop 0
	v_pk_mul_f32 v[68:69], v[70:71], v[68:69]
	s_nop 0
	v_cvt_pk_bf16_f32 v67, v68, v69
	global_store_dwordx2 v[234:235], v[66:67], off offset:96
.LBB0_1723:
	s_or_b64 exec, exec, s[12:13]
	v_add_u32_e32 v66, 0x80, v236
	v_cmp_gt_i32_e32 vcc, s28, v66
	s_and_saveexec_b64 s[12:13], vcc
	s_cbranch_execz .LBB0_1725
	v_mul_f32_e32 v68, 0xbfb8aa3b, v62
	v_mul_f32_e32 v69, 0xbfb8aa3b, v63
	v_exp_f32_e32 v68, v68
	v_exp_f32_e32 v69, v69
	v_add_u32_e32 v66, s29, v66
	v_ashrrev_i32_e32 v67, 31, v66
	v_lshlrev_b64 v[66:67], 10, v[66:67]
	v_pk_add_f32 v[68:69], v[68:69], 1.0 op_sel_hi:[1,0]
	v_lshl_add_u64 v[66:67], v[158:159], 0, v[66:67]
	v_rcp_f32_e32 v69, v69
	v_rcp_f32_e32 v68, v68
	s_nop 0
	v_pk_mul_f32 v[62:63], v[62:63], v[68:69]
	s_nop 0
	v_pk_mul_f32 v[58:59], v[62:63], v[58:59]
	v_mul_f32_e32 v62, 0xbfb8aa3b, v64
	v_mul_f32_e32 v63, 0xbfb8aa3b, v65
	v_exp_f32_e32 v62, v62
	v_exp_f32_e32 v63, v63
	v_cvt_pk_bf16_f32 v58, v58, v59
	v_pk_add_f32 v[62:63], v[62:63], 1.0 op_sel_hi:[1,0]
	s_nop 0
	v_rcp_f32_e32 v63, v63
	v_rcp_f32_e32 v62, v62
	s_nop 0
	v_pk_mul_f32 v[62:63], v[64:65], v[62:63]
	s_nop 0
	v_pk_mul_f32 v[60:61], v[62:63], v[60:61]
	s_nop 0
	v_cvt_pk_bf16_f32 v59, v60, v61
	global_store_dwordx2 v[66:67], v[58:59], off
	v_mul_f32_e32 v58, 0xbfb8aa3b, v54
	v_mul_f32_e32 v59, 0xbfb8aa3b, v55
	v_exp_f32_e32 v58, v58
	v_exp_f32_e32 v59, v59
	s_nop 0
	v_pk_add_f32 v[58:59], v[58:59], 1.0 op_sel_hi:[1,0]
	s_nop 0
	v_rcp_f32_e32 v59, v59
	v_rcp_f32_e32 v58, v58
	s_nop 0
	v_pk_mul_f32 v[54:55], v[54:55], v[58:59]
	s_nop 0
	v_pk_mul_f32 v[50:51], v[54:55], v[50:51]
	v_mul_f32_e32 v54, 0xbfb8aa3b, v56
	v_mul_f32_e32 v55, 0xbfb8aa3b, v57
	v_exp_f32_e32 v54, v54
	v_exp_f32_e32 v55, v55
	v_cvt_pk_bf16_f32 v50, v50, v51
	v_pk_add_f32 v[54:55], v[54:55], 1.0 op_sel_hi:[1,0]
	s_nop 0
	v_rcp_f32_e32 v55, v55
	v_rcp_f32_e32 v54, v54
	s_nop 0
	v_pk_mul_f32 v[54:55], v[56:57], v[54:55]
	s_nop 0
	v_pk_mul_f32 v[52:53], v[54:55], v[52:53]
	s_nop 0
	v_cvt_pk_bf16_f32 v51, v52, v53
	global_store_dwordx2 v[66:67], v[50:51], off offset:32
	v_mul_f32_e32 v50, 0xbfb8aa3b, v46
	v_mul_f32_e32 v51, 0xbfb8aa3b, v47
	v_exp_f32_e32 v50, v50
; DI unsigned pk2(float a, float b) { f32x2 v = {a, b}; bf16x2_t r = __builtin_convertvector(v, bf16x2_t); return __builtin_bit_cast(unsigned, r); }
; DI float sigmoidf_(float x) { return 1.f / (1.f + __expf(-x)); }
;     ...
; #pragma unroll
;             for (int mt = 0; mt < 3; ++mt) { const int tok = rp + wave * 48 + mt * 16 + tk;
;                 if (tok < M) {
;                     if (MODE == 0) { bf16* o = (bf16*)(ws + o_hid) + (size_t)(row0 + tok) * DEXP + slab * 64 + 4 * q;
; #pragma unroll
;                         for (int j = 0; j < 4; ++j) { float h[4];
; #pragma unroll
;                             for (int i = 0; i < 4; ++i) { const float gt = acc[mt][j][i]; h[i] = gt * sigmoidf_(gt) * acc[mt][j + 4][i]; }
;                             *(u32x2*)(o + 16 * j) = (u32x2){pk2(h[0], h[1]), pk2(h[2], h[3])}; }
	v_exp_f32_e32 v51, v51
	s_nop 0
	v_pk_add_f32 v[50:51], v[50:51], 1.0 op_sel_hi:[1,0]
	s_nop 0
	v_rcp_f32_e32 v51, v51
	v_rcp_f32_e32 v50, v50
	s_nop 0
	v_pk_mul_f32 v[46:47], v[46:47], v[50:51]
	s_nop 0
	v_pk_mul_f32 v[42:43], v[46:47], v[42:43]
	v_mul_f32_e32 v46, 0xbfb8aa3b, v48
	v_mul_f32_e32 v47, 0xbfb8aa3b, v49
	v_exp_f32_e32 v46, v46
	v_exp_f32_e32 v47, v47
	v_cvt_pk_bf16_f32 v42, v42, v43
	v_pk_add_f32 v[46:47], v[46:47], 1.0 op_sel_hi:[1,0]
	s_nop 0
	v_rcp_f32_e32 v47, v47
	v_rcp_f32_e32 v46, v46
	s_nop 0
	v_pk_mul_f32 v[46:47], v[48:49], v[46:47]
	s_nop 0
	v_pk_mul_f32 v[44:45], v[46:47], v[44:45]
	s_nop 0
	v_cvt_pk_bf16_f32 v43, v44, v45
	global_store_dwordx2 v[66:67], v[42:43], off offset:64
	v_mul_f32_e32 v42, 0xbfb8aa3b, v38
	v_mul_f32_e32 v43, 0xbfb8aa3b, v39
	v_exp_f32_e32 v42, v42
	v_exp_f32_e32 v43, v43
	s_nop 0
	v_pk_add_f32 v[42:43], v[42:43], 1.0 op_sel_hi:[1,0]
	s_nop 0
	v_rcp_f32_e32 v43, v43
	v_rcp_f32_e32 v42, v42
	s_nop 0
	v_pk_mul_f32 v[38:39], v[38:39], v[42:43]
	s_nop 0
	v_pk_mul_f32 v[34:35], v[38:39], v[34:35]
	v_mul_f32_e32 v38, 0xbfb8aa3b, v40
	v_mul_f32_e32 v39, 0xbfb8aa3b, v41
	v_exp_f32_e32 v38, v38
	v_exp_f32_e32 v39, v39
	v_cvt_pk_bf16_f32 v34, v34, v35
	v_pk_add_f32 v[38:39], v[38:39], 1.0 op_sel_hi:[1,0]
	s_nop 0
	v_rcp_f32_e32 v39, v39
	v_rcp_f32_e32 v38, v38
	s_nop 0
	v_pk_mul_f32 v[38:39], v[40:41], v[38:39]
	s_nop 0
	v_pk_mul_f32 v[36:37], v[38:39], v[36:37]
	s_nop 0
	v_cvt_pk_bf16_f32 v35, v36, v37
	global_store_dwordx2 v[66:67], v[34:35], off offset:96
.LBB0_1725:
	s_or_b64 exec, exec, s[12:13]
	v_add_u32_e32 v34, 0x100, v236
	v_cmp_gt_i32_e32 vcc, s28, v34
	s_and_saveexec_b64 s[12:13], vcc
	s_cbranch_execz .LBB0_1718
	v_mul_f32_e32 v36, 0xbfb8aa3b, v30
	v_mul_f32_e32 v37, 0xbfb8aa3b, v31
	v_exp_f32_e32 v36, v36
	v_exp_f32_e32 v37, v37
	v_add_u32_e32 v34, s29, v34
	v_ashrrev_i32_e32 v35, 31, v34
	v_lshlrev_b64 v[34:35], 10, v[34:35]
	v_pk_add_f32 v[36:37], v[36:37], 1.0 op_sel_hi:[1,0]
	v_lshl_add_u64 v[34:35], v[158:159], 0, v[34:35]
	v_rcp_f32_e32 v37, v37
	v_rcp_f32_e32 v36, v36
	s_nop 0
	v_pk_mul_f32 v[30:31], v[30:31], v[36:37]
	s_nop 0
	v_pk_mul_f32 v[26:27], v[30:31], v[26:27]
	v_mul_f32_e32 v30, 0xbfb8aa3b, v32
	v_mul_f32_e32 v31, 0xbfb8aa3b, v33
	v_exp_f32_e32 v30, v30
	v_exp_f32_e32 v31, v31
	v_cvt_pk_bf16_f32 v26, v26, v27
	v_pk_add_f32 v[30:31], v[30:31], 1.0 op_sel_hi:[1,0]
	s_nop 0
	v_rcp_f32_e32 v31, v31
	v_rcp_f32_e32 v30, v30
	s_nop 0
	v_pk_mul_f32 v[30:31], v[32:33], v[30:31]
	s_nop 0
	v_pk_mul_f32 v[28:29], v[30:31], v[28:29]
	s_nop 0
	v_cvt_pk_bf16_f32 v27, v28, v29
	global_store_dwordx2 v[34:35], v[26:27], off
	v_mul_f32_e32 v26, 0xbfb8aa3b, v22
	v_mul_f32_e32 v27, 0xbfb8aa3b, v23
	v_exp_f32_e32 v26, v26
	v_exp_f32_e32 v27, v27
	s_nop 0
	v_pk_add_f32 v[26:27], v[26:27], 1.0 op_sel_hi:[1,0]
	s_nop 0
	v_rcp_f32_e32 v27, v27
	v_rcp_f32_e32 v26, v26
	s_nop 0
	v_pk_mul_f32 v[22:23], v[22:23], v[26:27]
	s_nop 0
	v_pk_mul_f32 v[18:19], v[22:23], v[18:19]
	v_mul_f32_e32 v22, 0xbfb8aa3b, v24
	v_mul_f32_e32 v23, 0xbfb8aa3b, v25
	v_exp_f32_e32 v22, v22
	v_exp_f32_e32 v23, v23
	v_cvt_pk_bf16_f32 v18, v18, v19
	v_pk_add_f32 v[22:23], v[22:23], 1.0 op_sel_hi:[1,0]
	s_nop 0
	v_rcp_f32_e32 v23, v23
	v_rcp_f32_e32 v22, v22
	s_nop 0
	v_pk_mul_f32 v[22:23], v[24:25], v[22:23]
	s_nop 0
	v_pk_mul_f32 v[20:21], v[22:23], v[20:21]
	s_nop 0
	v_cvt_pk_bf16_f32 v19, v20, v21
	global_store_dwordx2 v[34:35], v[18:19], off offset:32
	v_mul_f32_e32 v18, 0xbfb8aa3b, v14
	v_mul_f32_e32 v19, 0xbfb8aa3b, v15
	v_exp_f32_e32 v18, v18
	v_exp_f32_e32 v19, v19
	s_nop 0
	v_pk_add_f32 v[18:19], v[18:19], 1.0 op_sel_hi:[1,0]
	s_nop 0
	v_rcp_f32_e32 v19, v19
	v_rcp_f32_e32 v18, v18
	s_nop 0
	v_pk_mul_f32 v[14:15], v[14:15], v[18:19]
	s_nop 0
	v_pk_mul_f32 v[10:11], v[14:15], v[10:11]
	v_mul_f32_e32 v14, 0xbfb8aa3b, v16
	v_mul_f32_e32 v15, 0xbfb8aa3b, v17
	v_exp_f32_e32 v14, v14
	v_exp_f32_e32 v15, v15
	v_cvt_pk_bf16_f32 v10, v10, v11
	v_pk_add_f32 v[14:15], v[14:15], 1.0 op_sel_hi:[1,0]
	s_nop 0
	v_rcp_f32_e32 v15, v15
	v_rcp_f32_e32 v14, v14
	s_nop 0
	v_pk_mul_f32 v[14:15], v[16:17], v[14:15]
	s_nop 0
	v_pk_mul_f32 v[12:13], v[14:15], v[12:13]
	s_nop 0
	v_cvt_pk_bf16_f32 v11, v12, v13
	global_store_dwordx2 v[34:35], v[10:11], off offset:64
	v_mul_f32_e32 v10, 0xbfb8aa3b, v6
	v_mul_f32_e32 v11, 0xbfb8aa3b, v7
	v_exp_f32_e32 v10, v10
	v_exp_f32_e32 v11, v11
	s_nop 0
	v_pk_add_f32 v[10:11], v[10:11], 1.0 op_sel_hi:[1,0]
	s_nop 0
	v_rcp_f32_e32 v11, v11
	v_rcp_f32_e32 v10, v10
	s_nop 0
	v_pk_mul_f32 v[6:7], v[6:7], v[10:11]
	s_nop 0
	v_pk_mul_f32 v[2:3], v[6:7], v[2:3]
	v_mul_f32_e32 v6, 0xbfb8aa3b, v8
	v_mul_f32_e32 v7, 0xbfb8aa3b, v9
	v_exp_f32_e32 v6, v6
	v_exp_f32_e32 v7, v7
	v_cvt_pk_bf16_f32 v2, v2, v3
	v_pk_add_f32 v[6:7], v[6:7], 1.0 op_sel_hi:[1,0]
	s_nop 0
	v_rcp_f32_e32 v7, v7
	v_rcp_f32_e32 v6, v6
	s_nop 0
	v_pk_mul_f32 v[6:7], v[8:9], v[6:7]
	s_nop 0
	v_pk_mul_f32 v[4:5], v[6:7], v[4:5]
	s_nop 0
	v_cvt_pk_bf16_f32 v3, v4, v5
	global_store_dwordx2 v[34:35], v[2:3], off offset:96
	s_branch .LBB0_1718
; __device__ __forceinline__ void xcd_barrier(const XcdBarrier& b) {
;     asm volatile("s_waitcnt vmcnt(0)" ::: "memory");
;     __syncthreads();
;     if (threadIdx.x == 0) {
;         unsigned* bar = b.bar;
;         __builtin_amdgcn_s_waitcnt(0);
;         unsigned nloc = b.st[0], nx = b.st[1];
;         if (nloc == 0u) { xcd_barrier_complete(bar, b.x, nloc, nx); b.st[0] = nloc; b.st[1] = nx; }
;     ...
;             f32x4 acc[3][8];
; #pragma unroll
;             for (int mt = 0; mt < 3; ++mt)
; #pragma unroll
;                 for (int j = 0; j < 8; ++j) acc[mt][j] = (f32x4){0.f, 0.f, 0.f, 0.f};
.Lxk_fast:
	s_mov_b32 s0, -2
	v_mov_b32_e32 v2, 0
	v_mov_b32_e32 v3, 0
	v_mov_b32_e32 v4, 0
	v_mov_b32_e32 v5, 0
	v_mov_b32_e32 v6, 0
	v_mov_b32_e32 v7, 0
	v_mov_b32_e32 v8, 0
	v_mov_b32_e32 v9, 0
	v_mov_b32_e32 v10, 0
	v_mov_b32_e32 v11, 0
	v_mov_b32_e32 v12, 0
	v_mov_b32_e32 v13, 0
	v_mov_b32_e32 v14, 0
	v_mov_b32_e32 v15, 0
	v_mov_b32_e32 v16, 0
	v_mov_b32_e32 v17, 0
	v_mov_b32_e32 v18, 0
	v_mov_b32_e32 v19, 0
	v_mov_b32_e32 v20, 0
	v_mov_b32_e32 v21, 0
	v_mov_b32_e32 v22, 0
	v_mov_b32_e32 v23, 0
	v_mov_b32_e32 v24, 0
	v_mov_b32_e32 v25, 0
	v_mov_b32_e32 v26, 0
	v_mov_b32_e32 v27, 0
	v_mov_b32_e32 v28, 0
	v_mov_b32_e32 v29, 0
	v_mov_b32_e32 v30, 0
	v_mov_b32_e32 v31, 0
	v_mov_b32_e32 v32, 0
	v_mov_b32_e32 v33, 0
	v_mov_b32_e32 v34, 0
	v_mov_b32_e32 v35, 0
	v_mov_b32_e32 v36, 0
	v_mov_b32_e32 v37, 0
	v_mov_b32_e32 v38, 0
	v_mov_b32_e32 v39, 0
	v_mov_b32_e32 v40, 0
	v_mov_b32_e32 v41, 0
	v_mov_b32_e32 v42, 0
	v_mov_b32_e32 v43, 0
	v_mov_b32_e32 v44, 0
	v_mov_b32_e32 v45, 0
	v_mov_b32_e32 v46, 0
	v_mov_b32_e32 v47, 0
	v_mov_b32_e32 v48, 0
	v_mov_b32_e32 v49, 0
	v_mov_b32_e32 v50, 0
	v_mov_b32_e32 v51, 0
	v_mov_b32_e32 v52, 0
	v_mov_b32_e32 v53, 0
	v_mov_b32_e32 v54, 0
	v_mov_b32_e32 v55, 0
	v_mov_b32_e32 v56, 0
	v_mov_b32_e32 v57, 0
	v_mov_b32_e32 v58, 0
	v_mov_b32_e32 v59, 0
	v_mov_b32_e32 v60, 0
	v_mov_b32_e32 v61, 0
	v_mov_b32_e32 v62, 0
	v_mov_b32_e32 v63, 0
	v_mov_b32_e32 v64, 0
	v_mov_b32_e32 v65, 0
	v_mov_b32_e32 v66, 0
	v_mov_b32_e32 v67, 0
	v_mov_b32_e32 v68, 0
	v_mov_b32_e32 v69, 0
	v_mov_b32_e32 v70, 0
	v_mov_b32_e32 v71, 0
	v_mov_b32_e32 v72, 0
	v_mov_b32_e32 v73, 0
	v_mov_b32_e32 v92, 0
	v_mov_b32_e32 v93, 0
	v_mov_b32_e32 v94, 0
	v_mov_b32_e32 v95, 0
	v_mov_b32_e32 v112, 0
	v_mov_b32_e32 v113, 0
	v_mov_b32_e32 v114, 0
	v_mov_b32_e32 v115, 0
	v_mov_b32_e32 v116, 0
	v_mov_b32_e32 v117, 0
	v_mov_b32_e32 v118, 0
	v_mov_b32_e32 v119, 0
	v_mov_b32_e32 v120, 0
	v_mov_b32_e32 v121, 0
	v_mov_b32_e32 v122, 0
	v_mov_b32_e32 v123, 0
	v_mov_b32_e32 v148, 0
	v_mov_b32_e32 v149, 0
	v_mov_b32_e32 v150, 0
	v_mov_b32_e32 v151, 0
	v_mov_b32_e32 v152, 0
	v_mov_b32_e32 v153, 0
	v_mov_b32_e32 v154, 0
	v_mov_b32_e32 v155, 0
	s_branch .Lxk_disp
.LBB0_1727:
	s_mov_b32 s10, 0x400000
	v_readlane_b32 s0, v255, 32
	s_add_i32 s0, s0, 10
	s_cmp_ge_i32 s0, s77
	s_cbranch_scc1 .LBB0_1777
	s_waitcnt vmcnt(0)
	s_barrier
	s_mov_b64 s[4:5], exec
	v_readlane_b32 s2, v255, 21
	v_readlane_b32 s3, v255, 22
	s_and_b64 s[2:3], s[4:5], s[2:3]
	s_mov_b64 exec, s[2:3]
	s_cbranch_execz .LBB0_1776
	v_readlane_b32 s1, v254, 0
	s_waitcnt vmcnt(0) expcnt(0) lgkmcnt(0)
	s_nop 0
	v_mov_b32_e32 v2, s1
	ds_read_b32 v4, v2
	ds_read_b32 v2, v2 offset:4
	s_waitcnt lgkmcnt(1)
	v_cmp_ne_u32_e32 vcc, 0, v4
	s_cbranch_vccnz .LBB0_1744
	s_load_dwordx2 s[2:3], s[78:79], 0x0
	s_load_dword s1, s[78:79], 0x8
	s_mov_b32 s7, 1
	s_waitcnt lgkmcnt(0)
	s_mul_i32 s2, s3, s2
	s_mul_i32 s1, s2, s1
	s_branch .LBB0_1732

;     ...
;         for (int rp = 0; rp < M; rp += 384) {
;             unsigned xso[6];
; #pragma unroll
;             for (int i = 0; i < 6; ++i) { int tok = rp + wave * 48 + 8 * i + (lane >> 3); tok = min(tok, M - 1); if (VAR == 5) tok &= 15; if (MODE == 0) tok = el[tok]; xso[i] = (unsigned)(tok * LDX * 2 + (lane & 7) * 16); }
.Lxl_none:
	s_mov_b32 s84, 0
	s_mov_b32 s85, 0x280000
	s_mov_b32 s86, 0
	s_mov_b32 s87, 0
	s_mov_b32 s88, 0
